# v47 + the s_setprio 0/1 flip in the middle of each 32-MFMA block removed in all six GEMM K-loops (priority stays raised across the whole block)
# baseline (speedup 1.0000x reference)
; #define PG8_STAGE(bufoff, gbase, voff) do { _Pragma("unroll") for (int _i = 0; _i < 2; ++_i) \
;         __builtin_amdgcn_global_load_lds((const unsigned*)((const char*)(gbase) + (voff)[_i]), (PG8_LAS unsigned*)(lds + (bufoff) + ldsw + _i * 8192), 16, 0, 0); } while (0)
; #define PG8_LDA(dst, b, h) do { _Pragma("unroll") for (int m = 0; m < 4; ++m) _Pragma("unroll") for (int k = 0; k < 2; ++k) dst[m][k] = *(const PG8_LAS bf16x8*)(lds + PG8_SA(b, h) + aoff + m * 2048 + k * 1024); } while (0)
; #define PG8_LDB(dst, b, h) do { _Pragma("unroll") for (int n = 0; n < 2; ++n) _Pragma("unroll") for (int k = 0; k < 2; ++k) dst[n][k] = *(const PG8_LAS bf16x8*)(lds + PG8_SB(b, h) + boff + n * 2048 + k * 1024); } while (0)
; #define PG8_MMA(ai, bj, At, Bt) do { __builtin_amdgcn_s_setprio(1); _Pragma("unroll") for (int m = 0; m < 4; ++m) _Pragma("unroll") for (int n = 0; n < 2; ++n) _Pragma("unroll") for (int k = 0; k < 2; ++k) \
;         acc[ai][bj][m][n] = __builtin_amdgcn_mfma_f32_16x16x32_bf16(Bt[n][k], At[m][k], acc[ai][bj][m][n], 0, 0, 0); __builtin_amdgcn_s_setprio(0); } while (0)
; #define PG8_WAIT_V(n) asm volatile("s_waitcnt vmcnt(" #n ")" ::: "memory")
; #define PG8_WAIT_L(n) asm volatile("s_waitcnt lgkmcnt(" #n ")" ::: "memory")
; #define PG8_BAR __builtin_amdgcn_s_barrier()
; #define PG8_BAR __builtin_amdgcn_s_barrier()
; template <class Epi, class Sched, bool ALIGN_EPI = false, bool SP2 = false>
; __device__ __forceinline__ void gemm_phase(PG8_LAS unsigned char* lds, const Gemm g, const Sched& S, const Epi& E, const int tid) {
;     ...
;         for (int t = 0; t < nt; t += 2) {
;             const bool last = (t == nt - 2);
;             const char* a1 = cA + (size_t)(t + 1) * kstep;
;             const char* a2 = last ? nA : cA + (size_t)(t + 2) * kstep; const char* b2 = last ? nB : cB + (size_t)(t + 2) * kstep;
;             const char* a3 = a2 + kstep; const char* b3 = b2 + kstep;
;             if (last && has_next) S.a_ready(nxt);
;             if constexpr (SP2) {
;             PG8_LDB(B0, 0, 0); PG8_LDB(B1, 0, 1); PG8_SCHED; PG8_LDA(At, 0, 0); PG8_STAGE(PG8_SA(1, 1), a1 + hstep, voffA);
;             PG8_WAIT_V(8); PG8_WAIT_L(0); PG8_BAR; PG8_MMA(0, 0, At, B0); PG8_MMA(0, 1, At, B1); PG8_BAR; PG8_SCHED;
;             PG8_LDA(At, 0, 1); PG8_STAGE(PG8_SB(0, 0), b2, voffB); PG8_STAGE(PG8_SB(0, 1), b2 + hstep, voffB); PG8_STAGE(PG8_SA(0, 0), a2, voffA);
.LBB0_757:
	s_add_u32 s6, s40, 0xfff80080
	s_addc_u32 s7, s41, -1
	s_add_i32 s15, 0, 0x10000
	s_cmp_eq_u32 s13, 28
	s_cselect_b32 s69, s1, s7
	s_cselect_b32 s68, s2, s6
	v_add_u32_e32 v131, s15, v152
	s_cselect_b32 s7, s5, s12
	s_cselect_b32 s6, s10, s11
	s_add_i32 s16, 0, 0x14000
	ds_read_b128 v[164:167], v131
	ds_read_b128 v[168:171], v131 offset:1024
	ds_read_b128 v[172:175], v131 offset:2048
	ds_read_b128 v[176:179], v131 offset:3072
	v_add_u32_e32 v131, s16, v152
	ds_read_b128 v[180:183], v131
	ds_read_b128 v[184:187], v131 offset:1024
	ds_read_b128 v[188:191], v131 offset:2048
	ds_read_b128 v[192:195], v131 offset:3072
	v_lshl_add_u64 v[132:133], s[40:41], 0, v[144:145]
	s_add_i32 m0, s46, 0xc000
	ds_read_b128 v[198:201], v163
	ds_read_b128 v[202:205], v163 offset:1024
	ds_read_b128 v[206:209], v163 offset:2048
	ds_read_b128 v[210:213], v163 offset:3072
	ds_read_b128 v[214:217], v163 offset:4096
	ds_read_b128 v[218:221], v163 offset:5120
	ds_read_b128 v[222:225], v163 offset:6144
	ds_read_b128 v[226:229], v163 offset:7168
	global_load_lds_dwordx4 v[132:133], off
	v_lshl_add_u64 v[132:133], s[40:41], 0, v[146:147]
	s_add_i32 m0, s46, 0xe000
	s_nop 0
	global_load_lds_dwordx4 v[132:133], off
	s_waitcnt vmcnt(8)
	s_waitcnt lgkmcnt(0)
	s_barrier
	s_setprio 1
	s_waitcnt lgkmcnt(0)
	v_mfma_f32_16x16x32_bf16 v[126:129], v[164:167], v[198:201], v[126:129]
	v_mfma_f32_16x16x32_bf16 v[122:125], v[172:175], v[198:201], v[122:125]
	v_mfma_f32_16x16x32_bf16 v[118:121], v[164:167], v[206:209], v[118:121]
	v_mfma_f32_16x16x32_bf16 v[110:113], v[172:175], v[206:209], v[110:113]
	v_mfma_f32_16x16x32_bf16 v[102:105], v[164:167], v[214:217], v[102:105]
	v_mfma_f32_16x16x32_bf16 v[94:97], v[172:175], v[214:217], v[94:97]
	v_mfma_f32_16x16x32_bf16 v[86:89], v[164:167], v[222:225], v[86:89]
	v_mfma_f32_16x16x32_bf16 v[78:81], v[172:175], v[222:225], v[78:81]
	v_mfma_f32_16x16x32_bf16 v[126:129], v[168:171], v[202:205], v[126:129]
	v_mfma_f32_16x16x32_bf16 v[122:125], v[176:179], v[202:205], v[122:125]
	v_mfma_f32_16x16x32_bf16 v[118:121], v[168:171], v[210:213], v[118:121]
	v_mfma_f32_16x16x32_bf16 v[110:113], v[176:179], v[210:213], v[110:113]
	v_mfma_f32_16x16x32_bf16 v[102:105], v[168:171], v[218:221], v[102:105]
	v_mfma_f32_16x16x32_bf16 v[94:97], v[176:179], v[218:221], v[94:97]
	v_mfma_f32_16x16x32_bf16 v[86:89], v[168:171], v[226:229], v[86:89]
	v_mfma_f32_16x16x32_bf16 v[78:81], v[176:179], v[226:229], v[78:81]
	v_mfma_f32_16x16x32_bf16 v[114:117], v[180:183], v[198:201], v[114:117]
	v_mfma_f32_16x16x32_bf16 v[106:109], v[188:191], v[198:201], v[106:109]
	v_mfma_f32_16x16x32_bf16 v[98:101], v[180:183], v[206:209], v[98:101]
	v_mfma_f32_16x16x32_bf16 v[90:93], v[188:191], v[206:209], v[90:93]
	v_mfma_f32_16x16x32_bf16 v[82:85], v[180:183], v[214:217], v[82:85]
	v_mfma_f32_16x16x32_bf16 v[74:77], v[188:191], v[214:217], v[74:77]
	v_mfma_f32_16x16x32_bf16 v[70:73], v[180:183], v[222:225], v[70:73]
	v_mfma_f32_16x16x32_bf16 v[66:69], v[188:191], v[222:225], v[66:69]
	v_mfma_f32_16x16x32_bf16 v[114:117], v[184:187], v[202:205], v[114:117]
	v_mfma_f32_16x16x32_bf16 v[106:109], v[192:195], v[202:205], v[106:109]
	v_mfma_f32_16x16x32_bf16 v[98:101], v[184:187], v[210:213], v[98:101]
	v_mfma_f32_16x16x32_bf16 v[90:93], v[192:195], v[210:213], v[90:93]
	v_mfma_f32_16x16x32_bf16 v[82:85], v[184:187], v[218:221], v[82:85]
	v_mfma_f32_16x16x32_bf16 v[74:77], v[192:195], v[218:221], v[74:77]
	v_mfma_f32_16x16x32_bf16 v[70:73], v[184:187], v[226:229], v[70:73]
	v_mfma_f32_16x16x32_bf16 v[66:69], v[192:195], v[226:229], v[66:69]
	s_setprio 0
	s_barrier
	s_add_i32 s15, s15, s49
	v_lshl_add_u64 v[132:133], s[6:7], 0, v[136:137]
	s_mov_b32 m0, s15
	ds_read_b128 v[198:201], v163 offset:16384
	ds_read_b128 v[202:205], v163 offset:17408
	ds_read_b128 v[206:209], v163 offset:18432
	ds_read_b128 v[210:213], v163 offset:19456
	ds_read_b128 v[214:217], v163 offset:20480
	ds_read_b128 v[218:221], v163 offset:21504
	ds_read_b128 v[222:225], v163 offset:22528
	ds_read_b128 v[226:229], v163 offset:23552
	global_load_lds_dwordx4 v[132:133], off
	s_add_i32 m0, s15, 0x2000
	s_add_u32 s18, s6, 0x80000
	v_lshl_add_u64 v[148:149], s[6:7], 0, v[140:141]
	s_addc_u32 s19, s7, 0
	s_add_i32 s15, s16, s49
	global_load_lds_dwordx4 v[148:149], off
	v_lshl_add_u64 v[230:231], s[18:19], 0, v[136:137]
	s_mov_b32 m0, s15
	v_lshl_add_u64 v[242:243], s[68:69], 0, v[138:139]
	global_load_lds_dwordx4 v[230:231], off
	v_lshl_add_u64 v[230:231], s[18:19], 0, v[140:141]
	s_add_i32 m0, s15, 0x2000
	s_nop 0
	global_load_lds_dwordx4 v[230:231], off
	v_lshl_add_u64 v[230:231], s[68:69], 0, v[134:135]
	s_mov_b32 m0, s46
	s_nop 0
	global_load_lds_dwordx4 v[230:231], off
	s_mov_b32 m0, s47
	s_nop 0
	global_load_lds_dwordx4 v[242:243], off
	s_waitcnt vmcnt(8)
	s_waitcnt lgkmcnt(0)
	s_barrier
; #define PG8_STAGE(bufoff, gbase, voff) do { _Pragma("unroll") for (int _i = 0; _i < 2; ++_i) \
;         __builtin_amdgcn_global_load_lds((const unsigned*)((const char*)(gbase) + (voff)[_i]), (PG8_LAS unsigned*)(lds + (bufoff) + ldsw + _i * 8192), 16, 0, 0); } while (0)
; #define PG8_LDA(dst, b, h) do { _Pragma("unroll") for (int m = 0; m < 4; ++m) _Pragma("unroll") for (int k = 0; k < 2; ++k) dst[m][k] = *(const PG8_LAS bf16x8*)(lds + PG8_SA(b, h) + aoff + m * 2048 + k * 1024); } while (0)
; #define PG8_LDB(dst, b, h) do { _Pragma("unroll") for (int n = 0; n < 2; ++n) _Pragma("unroll") for (int k = 0; k < 2; ++k) dst[n][k] = *(const PG8_LAS bf16x8*)(lds + PG8_SB(b, h) + boff + n * 2048 + k * 1024); } while (0)
; #define PG8_MMA(ai, bj, At, Bt) do { __builtin_amdgcn_s_setprio(1); _Pragma("unroll") for (int m = 0; m < 4; ++m) _Pragma("unroll") for (int n = 0; n < 2; ++n) _Pragma("unroll") for (int k = 0; k < 2; ++k) \
;         acc[ai][bj][m][n] = __builtin_amdgcn_mfma_f32_16x16x32_bf16(Bt[n][k], At[m][k], acc[ai][bj][m][n], 0, 0, 0); __builtin_amdgcn_s_setprio(0); } while (0)
; #define PG8_WAIT_V(n) asm volatile("s_waitcnt vmcnt(" #n ")" ::: "memory")
; #define PG8_WAIT_L(n) asm volatile("s_waitcnt lgkmcnt(" #n ")" ::: "memory")
; #define PG8_BAR __builtin_amdgcn_s_barrier()
; #define PG8_SCHED __builtin_amdgcn_sched_barrier(0)
; #define PG8_STAGE(bufoff, gbase, voff) do { _Pragma("unroll") for (int _i = 0; _i < 2; ++_i) \
;         __builtin_amdgcn_global_load_lds((const unsigned*)((const char*)(gbase) + (voff)[_i]), (PG8_LAS unsigned*)(lds + (bufoff) + ldsw + _i * 8192), 16, 0, 0); } while (0)
; #define PG8_WAIT_V(n) asm volatile("s_waitcnt vmcnt(" #n ")" ::: "memory")
; #define PG8_WAIT_L(n) asm volatile("s_waitcnt lgkmcnt(" #n ")" ::: "memory")
; template <class Epi, class Sched, bool ALIGN_EPI = false, bool SP2 = false>
; __device__ __forceinline__ void gemm_phase(PG8_LAS unsigned char* lds, const Gemm g, const Sched& S, const Epi& E, const int tid) {
;     ...
;             PG8_WAIT_V(8); PG8_WAIT_L(0); PG8_BAR; PG8_MMA(1, 0, At, B0); PG8_MMA(1, 1, At, B1); PG8_BAR; PG8_SCHED;
;             PG8_LDB(B0, 1, 0); PG8_LDB(B1, 1, 1); PG8_SCHED; PG8_LDA(At, 1, 0); PG8_STAGE(PG8_SA(0, 1), a2 + hstep, voffA);
;             PG8_WAIT_V(8); PG8_WAIT_L(0); PG8_BAR; PG8_MMA(0, 0, At, B0); PG8_MMA(0, 1, At, B1); PG8_BAR; PG8_SCHED;
	s_setprio 1
	s_waitcnt lgkmcnt(0)
	v_mfma_f32_16x16x32_bf16 v[62:65], v[164:167], v[198:201], v[62:65]
	v_mfma_f32_16x16x32_bf16 v[58:61], v[172:175], v[198:201], v[58:61]
	v_mfma_f32_16x16x32_bf16 v[54:57], v[164:167], v[206:209], v[54:57]
	v_mfma_f32_16x16x32_bf16 v[46:49], v[172:175], v[206:209], v[46:49]
	v_mfma_f32_16x16x32_bf16 v[38:41], v[164:167], v[214:217], v[38:41]
	v_mfma_f32_16x16x32_bf16 v[30:33], v[172:175], v[214:217], v[30:33]
	v_mfma_f32_16x16x32_bf16 v[22:25], v[164:167], v[222:225], v[22:25]
	v_mfma_f32_16x16x32_bf16 v[14:17], v[172:175], v[222:225], v[14:17]
	v_mfma_f32_16x16x32_bf16 v[62:65], v[168:171], v[202:205], v[62:65]
	v_mfma_f32_16x16x32_bf16 v[58:61], v[176:179], v[202:205], v[58:61]
	v_mfma_f32_16x16x32_bf16 v[54:57], v[168:171], v[210:213], v[54:57]
	v_mfma_f32_16x16x32_bf16 v[46:49], v[176:179], v[210:213], v[46:49]
	v_mfma_f32_16x16x32_bf16 v[38:41], v[168:171], v[218:221], v[38:41]
	v_mfma_f32_16x16x32_bf16 v[30:33], v[176:179], v[218:221], v[30:33]
	v_mfma_f32_16x16x32_bf16 v[22:25], v[168:171], v[226:229], v[22:25]
	v_mfma_f32_16x16x32_bf16 v[14:17], v[176:179], v[226:229], v[14:17]
	v_mfma_f32_16x16x32_bf16 v[50:53], v[180:183], v[198:201], v[50:53]
	v_mfma_f32_16x16x32_bf16 v[42:45], v[188:191], v[198:201], v[42:45]
	v_mfma_f32_16x16x32_bf16 v[34:37], v[180:183], v[206:209], v[34:37]
	v_mfma_f32_16x16x32_bf16 v[26:29], v[188:191], v[206:209], v[26:29]
	v_mfma_f32_16x16x32_bf16 v[18:21], v[180:183], v[214:217], v[18:21]
	v_mfma_f32_16x16x32_bf16 v[10:13], v[188:191], v[214:217], v[10:13]
	v_mfma_f32_16x16x32_bf16 v[6:9], v[180:183], v[222:225], v[6:9]
	v_mfma_f32_16x16x32_bf16 v[2:5], v[188:191], v[222:225], v[2:5]
	v_mfma_f32_16x16x32_bf16 v[50:53], v[184:187], v[202:205], v[50:53]
	v_mfma_f32_16x16x32_bf16 v[42:45], v[192:195], v[202:205], v[42:45]
	v_mfma_f32_16x16x32_bf16 v[34:37], v[184:187], v[210:213], v[34:37]
	v_mfma_f32_16x16x32_bf16 v[26:29], v[192:195], v[210:213], v[26:29]
	v_mfma_f32_16x16x32_bf16 v[18:21], v[184:187], v[218:221], v[18:21]
	v_mfma_f32_16x16x32_bf16 v[10:13], v[192:195], v[218:221], v[10:13]
	v_mfma_f32_16x16x32_bf16 v[6:9], v[184:187], v[226:229], v[6:9]
	v_mfma_f32_16x16x32_bf16 v[2:5], v[192:195], v[226:229], v[2:5]
	s_setprio 0
	s_barrier
	s_add_i32 s15, 0, 0x18000
	v_add_u32_e32 v131, s15, v152
	s_add_i32 s16, 0, 0x1c000
	ds_read_b128 v[164:167], v131
	ds_read_b128 v[168:171], v131 offset:1024
	ds_read_b128 v[172:175], v131 offset:2048
	ds_read_b128 v[176:179], v131 offset:3072
	v_add_u32_e32 v131, s16, v152
	ds_read_b128 v[180:183], v131
	ds_read_b128 v[184:187], v131 offset:1024
	ds_read_b128 v[188:191], v131 offset:2048
	ds_read_b128 v[192:195], v131 offset:3072
	s_add_u32 s18, s68, 0x80000
	s_addc_u32 s19, s69, 0
	s_mov_b32 m0, s44
	v_lshl_add_u64 v[244:245], s[18:19], 0, v[134:135]
	ds_read_b128 v[198:201], v163 offset:32768
	ds_read_b128 v[202:205], v163 offset:33792
	ds_read_b128 v[206:209], v163 offset:34816
	ds_read_b128 v[210:213], v163 offset:35840
	ds_read_b128 v[214:217], v163 offset:36864
	ds_read_b128 v[218:221], v163 offset:37888
	ds_read_b128 v[222:225], v163 offset:38912
	ds_read_b128 v[226:229], v163 offset:39936
	global_load_lds_dwordx4 v[244:245], off
	v_lshl_add_u64 v[244:245], s[18:19], 0, v[138:139]
	s_mov_b32 m0, s45
	s_nop 0
	global_load_lds_dwordx4 v[244:245], off
	s_waitcnt vmcnt(8)
	s_waitcnt lgkmcnt(0)
	s_barrier
	s_setprio 1
	s_waitcnt lgkmcnt(0)
	v_mfma_f32_16x16x32_bf16 v[126:129], v[164:167], v[198:201], v[126:129]
	v_mfma_f32_16x16x32_bf16 v[122:125], v[172:175], v[198:201], v[122:125]
	v_mfma_f32_16x16x32_bf16 v[118:121], v[164:167], v[206:209], v[118:121]
	v_mfma_f32_16x16x32_bf16 v[110:113], v[172:175], v[206:209], v[110:113]
	v_mfma_f32_16x16x32_bf16 v[102:105], v[164:167], v[214:217], v[102:105]
	v_mfma_f32_16x16x32_bf16 v[94:97], v[172:175], v[214:217], v[94:97]
	v_mfma_f32_16x16x32_bf16 v[86:89], v[164:167], v[222:225], v[86:89]
	v_mfma_f32_16x16x32_bf16 v[78:81], v[172:175], v[222:225], v[78:81]
	v_mfma_f32_16x16x32_bf16 v[126:129], v[168:171], v[202:205], v[126:129]
	v_mfma_f32_16x16x32_bf16 v[122:125], v[176:179], v[202:205], v[122:125]
	v_mfma_f32_16x16x32_bf16 v[118:121], v[168:171], v[210:213], v[118:121]
	v_mfma_f32_16x16x32_bf16 v[110:113], v[176:179], v[210:213], v[110:113]
	v_mfma_f32_16x16x32_bf16 v[102:105], v[168:171], v[218:221], v[102:105]
	v_mfma_f32_16x16x32_bf16 v[94:97], v[176:179], v[218:221], v[94:97]
	v_mfma_f32_16x16x32_bf16 v[86:89], v[168:171], v[226:229], v[86:89]
	v_mfma_f32_16x16x32_bf16 v[78:81], v[176:179], v[226:229], v[78:81]
	v_mfma_f32_16x16x32_bf16 v[114:117], v[180:183], v[198:201], v[114:117]
	v_mfma_f32_16x16x32_bf16 v[106:109], v[188:191], v[198:201], v[106:109]
	v_mfma_f32_16x16x32_bf16 v[98:101], v[180:183], v[206:209], v[98:101]
	v_mfma_f32_16x16x32_bf16 v[90:93], v[188:191], v[206:209], v[90:93]
	v_mfma_f32_16x16x32_bf16 v[82:85], v[180:183], v[214:217], v[82:85]
	v_mfma_f32_16x16x32_bf16 v[74:77], v[188:191], v[214:217], v[74:77]
	v_mfma_f32_16x16x32_bf16 v[70:73], v[180:183], v[222:225], v[70:73]
	v_mfma_f32_16x16x32_bf16 v[66:69], v[188:191], v[222:225], v[66:69]
	v_mfma_f32_16x16x32_bf16 v[114:117], v[184:187], v[202:205], v[114:117]
	v_mfma_f32_16x16x32_bf16 v[106:109], v[192:195], v[202:205], v[106:109]
	v_mfma_f32_16x16x32_bf16 v[98:101], v[184:187], v[210:213], v[98:101]
	v_mfma_f32_16x16x32_bf16 v[90:93], v[192:195], v[210:213], v[90:93]
	v_mfma_f32_16x16x32_bf16 v[82:85], v[184:187], v[218:221], v[82:85]
	v_mfma_f32_16x16x32_bf16 v[74:77], v[192:195], v[218:221], v[74:77]
	v_mfma_f32_16x16x32_bf16 v[70:73], v[184:187], v[226:229], v[70:73]
	v_mfma_f32_16x16x32_bf16 v[66:69], v[192:195], v[226:229], v[66:69]
	s_setprio 0
	s_barrier
; #define PG8_STAGE(bufoff, gbase, voff) do { _Pragma("unroll") for (int _i = 0; _i < 2; ++_i) \
;         __builtin_amdgcn_global_load_lds((const unsigned*)((const char*)(gbase) + (voff)[_i]), (PG8_LAS unsigned*)(lds + (bufoff) + ldsw + _i * 8192), 16, 0, 0); } while (0)
; #define PG8_LDA(dst, b, h) do { _Pragma("unroll") for (int m = 0; m < 4; ++m) _Pragma("unroll") for (int k = 0; k < 2; ++k) dst[m][k] = *(const PG8_LAS bf16x8*)(lds + PG8_SA(b, h) + aoff + m * 2048 + k * 1024); } while (0)
; #define PG8_MMA(ai, bj, At, Bt) do { __builtin_amdgcn_s_setprio(1); _Pragma("unroll") for (int m = 0; m < 4; ++m) _Pragma("unroll") for (int n = 0; n < 2; ++n) _Pragma("unroll") for (int k = 0; k < 2; ++k) \
;         acc[ai][bj][m][n] = __builtin_amdgcn_mfma_f32_16x16x32_bf16(Bt[n][k], At[m][k], acc[ai][bj][m][n], 0, 0, 0); __builtin_amdgcn_s_setprio(0); } while (0)
; #define PG8_WAIT_V(n) asm volatile("s_waitcnt vmcnt(" #n ")" ::: "memory")
; #define PG8_WAIT_L(n) asm volatile("s_waitcnt lgkmcnt(" #n ")" ::: "memory")
; #define PG8_BAR __builtin_amdgcn_s_barrier()
; #define PG8_SCHED __builtin_amdgcn_sched_barrier(0)
; #define PG8_STAGE(bufoff, gbase, voff) do { _Pragma("unroll") for (int _i = 0; _i < 2; ++_i) \
;         __builtin_amdgcn_global_load_lds((const unsigned*)((const char*)(gbase) + (voff)[_i]), (PG8_LAS unsigned*)(lds + (bufoff) + ldsw + _i * 8192), 16, 0, 0); } while (0)
; #define PG8_LDA(dst, b, h) do { _Pragma("unroll") for (int mb = 0; mb < 2; ++mb) _Pragma("unroll") for (int s = 0; s < 2; ++s) \
;         dst[mb][s] = cat8(*(const PG8_LAS bf16x8*)(lds + PG8_SA(b, h) + aoffk[s][0] + mb * 4096), *(const PG8_LAS bf16x8*)(lds + PG8_SA(b, h) + aoffk[s][1] + mb * 4096)); } while (0)
; #define PG8_WAIT_V(n) asm volatile("s_waitcnt vmcnt(" #n ")" ::: "memory")
; template <class Epi, class Sched, bool ALIGN_EPI = false, bool SP2 = false>
; __device__ __forceinline__ void gemm_phase(PG8_LAS unsigned char* lds, const Gemm g, const Sched& S, const Epi& E, const int tid) {
;     ...
;         for (int t = 0; t < nt; t += 2) {
;             const bool last = (t == nt - 2);
;     ...
;             PG8_LDA(At, 1, 1); PG8_STAGE(PG8_SB(1, 0), b3, voffB); PG8_STAGE(PG8_SB(1, 1), b3 + hstep, voffB); PG8_STAGE(PG8_SA(1, 0), a3, voffA);
;             PG8_WAIT_V(8); PG8_WAIT_L(0); PG8_BAR; PG8_MMA(1, 0, At, B0); PG8_MMA(1, 1, At, B1); PG8_BAR; PG8_SCHED;
	s_add_i32 s15, s15, s49
	v_lshl_add_u64 v[132:133], v[132:133], 0, s[34:35]
	s_mov_b32 m0, s15
	ds_read_b128 v[198:201], v163 offset:49152
	ds_read_b128 v[202:205], v163 offset:50176
	ds_read_b128 v[206:209], v163 offset:51200
	ds_read_b128 v[210:213], v163 offset:52224
	ds_read_b128 v[214:217], v163 offset:53248
	ds_read_b128 v[218:221], v163 offset:54272
	ds_read_b128 v[222:225], v163 offset:55296
	ds_read_b128 v[226:229], v163 offset:56320
	global_load_lds_dwordx4 v[132:133], off
	s_add_i32 m0, s15, 0x2000
	s_add_u32 s6, s6, 0x80080
	v_lshl_add_u64 v[132:133], v[148:149], 0, s[34:35]
	s_addc_u32 s7, s7, 0
	s_add_i32 s15, s16, s49
	global_load_lds_dwordx4 v[132:133], off
	v_lshl_add_u64 v[132:133], s[6:7], 0, v[136:137]
	s_mov_b32 m0, s15
	s_nop 0
	global_load_lds_dwordx4 v[132:133], off
	v_lshl_add_u64 v[132:133], s[6:7], 0, v[140:141]
	s_add_i32 m0, s15, 0x2000
	s_nop 0
	global_load_lds_dwordx4 v[132:133], off
	v_lshl_add_u64 v[132:133], v[230:231], 0, s[34:35]
	s_mov_b32 m0, s54
	s_nop 0
	global_load_lds_dwordx4 v[132:133], off
	v_lshl_add_u64 v[132:133], v[242:243], 0, s[34:35]
	s_mov_b32 m0, s55
	s_nop 0
	global_load_lds_dwordx4 v[132:133], off
	s_waitcnt vmcnt(8)
	s_waitcnt lgkmcnt(0)
	s_barrier
	s_setprio 1
	s_waitcnt lgkmcnt(0)
	v_mfma_f32_16x16x32_bf16 v[62:65], v[164:167], v[198:201], v[62:65]
	v_mfma_f32_16x16x32_bf16 v[58:61], v[172:175], v[198:201], v[58:61]
	v_mfma_f32_16x16x32_bf16 v[54:57], v[164:167], v[206:209], v[54:57]
	v_mfma_f32_16x16x32_bf16 v[46:49], v[172:175], v[206:209], v[46:49]
	v_mfma_f32_16x16x32_bf16 v[38:41], v[164:167], v[214:217], v[38:41]
	v_mfma_f32_16x16x32_bf16 v[30:33], v[172:175], v[214:217], v[30:33]
	v_mfma_f32_16x16x32_bf16 v[22:25], v[164:167], v[222:225], v[22:25]
	v_mfma_f32_16x16x32_bf16 v[14:17], v[172:175], v[222:225], v[14:17]
	v_mfma_f32_16x16x32_bf16 v[62:65], v[168:171], v[202:205], v[62:65]
	v_mfma_f32_16x16x32_bf16 v[58:61], v[176:179], v[202:205], v[58:61]
	v_mfma_f32_16x16x32_bf16 v[54:57], v[168:171], v[210:213], v[54:57]
	v_mfma_f32_16x16x32_bf16 v[46:49], v[176:179], v[210:213], v[46:49]
	v_mfma_f32_16x16x32_bf16 v[38:41], v[168:171], v[218:221], v[38:41]
	v_mfma_f32_16x16x32_bf16 v[30:33], v[176:179], v[218:221], v[30:33]
	v_mfma_f32_16x16x32_bf16 v[22:25], v[168:171], v[226:229], v[22:25]
	v_mfma_f32_16x16x32_bf16 v[14:17], v[176:179], v[226:229], v[14:17]
	v_mfma_f32_16x16x32_bf16 v[50:53], v[180:183], v[198:201], v[50:53]
	v_mfma_f32_16x16x32_bf16 v[42:45], v[188:191], v[198:201], v[42:45]
	v_mfma_f32_16x16x32_bf16 v[34:37], v[180:183], v[206:209], v[34:37]
	v_mfma_f32_16x16x32_bf16 v[26:29], v[188:191], v[206:209], v[26:29]
	v_mfma_f32_16x16x32_bf16 v[18:21], v[180:183], v[214:217], v[18:21]
	v_mfma_f32_16x16x32_bf16 v[10:13], v[188:191], v[214:217], v[10:13]
	v_mfma_f32_16x16x32_bf16 v[6:9], v[180:183], v[222:225], v[6:9]
	v_mfma_f32_16x16x32_bf16 v[2:5], v[188:191], v[222:225], v[2:5]
	v_mfma_f32_16x16x32_bf16 v[50:53], v[184:187], v[202:205], v[50:53]
	v_mfma_f32_16x16x32_bf16 v[42:45], v[192:195], v[202:205], v[42:45]
	v_mfma_f32_16x16x32_bf16 v[34:37], v[184:187], v[210:213], v[34:37]
	v_mfma_f32_16x16x32_bf16 v[26:29], v[192:195], v[210:213], v[26:29]
	v_mfma_f32_16x16x32_bf16 v[18:21], v[184:187], v[218:221], v[18:21]
	v_mfma_f32_16x16x32_bf16 v[10:13], v[192:195], v[218:221], v[10:13]
	v_mfma_f32_16x16x32_bf16 v[6:9], v[184:187], v[226:229], v[6:9]
	v_mfma_f32_16x16x32_bf16 v[2:5], v[192:195], v[226:229], v[2:5]
	s_setprio 0
	s_barrier
	s_add_i32 s13, s13, 2
	s_add_u32 s40, s40, 0x100
	s_addc_u32 s41, s41, 0
	s_add_u32 s11, s11, 0x100
	s_addc_u32 s12, s12, 0
	s_cmp_gt_u32 s13, 29
	s_cbranch_scc0 .LBB0_757
	s_and_b64 vcc, exec, s[70:71]
	s_cbranch_vccz .LBB0_760
	s_barrier

; #define PG8_STAGE(bufoff, gbase, voff) do { _Pragma("unroll") for (int _i = 0; _i < 2; ++_i) \
;         __builtin_amdgcn_global_load_lds((const unsigned*)((const char*)(gbase) + (voff)[_i]), (PG8_LAS unsigned*)(lds + (bufoff) + ldsw + _i * 8192), 16, 0, 0); } while (0)
; #define PG8_LDA(dst, b, h) do { _Pragma("unroll") for (int m = 0; m < 4; ++m) _Pragma("unroll") for (int k = 0; k < 2; ++k) dst[m][k] = *(const PG8_LAS bf16x8*)(lds + PG8_SA(b, h) + aoff + m * 2048 + k * 1024); } while (0)
; #define PG8_LDB(dst, b, h) do { _Pragma("unroll") for (int n = 0; n < 2; ++n) _Pragma("unroll") for (int k = 0; k < 2; ++k) dst[n][k] = *(const PG8_LAS bf16x8*)(lds + PG8_SB(b, h) + boff + n * 2048 + k * 1024); } while (0)
; #define PG8_WAIT_V(n) asm volatile("s_waitcnt vmcnt(" #n ")" ::: "memory")
; #define PG8_WAIT_L(n) asm volatile("s_waitcnt lgkmcnt(" #n ")" ::: "memory")
; #define PG8_BAR __builtin_amdgcn_s_barrier()
; #define PG8_SCHED __builtin_amdgcn_sched_barrier(0)
; #define PG8_BAR __builtin_amdgcn_s_barrier()
; template <class Epi, class Sched, bool ALIGN_EPI = false, bool SP2 = false>
; __device__ __forceinline__ void gemm_phase(PG8_LAS unsigned char* lds, const Gemm g, const Sched& S, const Epi& E, const int tid) {
;     ...
;         const char* nA = has_next ? (const char*)g.A + (size_t)nxt.pm * tstep + (size_t)nxt.k0 * 2 : cA; const char* nB = has_next ? (const char*)g.Bt + (size_t)nxt.pn * tstep + (size_t)nxt.k0 * 2 : cB;
;         for (int t = 0; t < nt; t += 2) {
;             const bool last = (t == nt - 2);
;             const char* a1 = cA + (size_t)(t + 1) * kstep;
;             const char* a2 = last ? nA : cA + (size_t)(t + 2) * kstep; const char* b2 = last ? nB : cB + (size_t)(t + 2) * kstep;
;             const char* a3 = a2 + kstep; const char* b3 = b2 + kstep;
;             if (last && has_next) S.a_ready(nxt);
;             if constexpr (SP2) {
;             PG8_LDB(B0, 0, 0); PG8_LDB(B1, 0, 1); PG8_SCHED; PG8_LDA(At, 0, 0); PG8_STAGE(PG8_SA(1, 1), a1 + hstep, voffA);
;             PG8_WAIT_V(8); PG8_WAIT_L(0); PG8_BAR; PG8_MMA(0, 0, At, B0); PG8_MMA(0, 1, At, B1); PG8_BAR; PG8_SCHED;
;             PG8_LDA(At, 0, 1); PG8_STAGE(PG8_SB(0, 0), b2, voffB); PG8_STAGE(PG8_SB(0, 1), b2 + hstep, voffB); PG8_STAGE(PG8_SA(0, 0), a2, voffA);
;             PG8_WAIT_V(8); PG8_WAIT_L(0); PG8_BAR; PG8_MMA(1, 0, At, B0); PG8_MMA(1, 1, At, B1); PG8_BAR; PG8_SCHED;
.LBB0_1589:
	s_add_i32 s63, s6, 2
	s_add_u32 s7, s46, 0xfff80080
	s_addc_u32 s48, s47, -1
	s_add_i32 s65, 0, 0x10000
	s_cmp_eq_u32 s23, s6
	s_cselect_b32 s49, s12, s48
	s_cselect_b32 s48, s13, s7
	s_cselect_b32 s7, s17, s45
	s_cselect_b32 s6, s21, s39
	s_add_i32 s68, 0, 0x14000
	v_add_u32_e32 v144, s65, v180
	v_add_u32_e32 v160, s68, v180
	ds_read_b128 v[132:135], v144
	ds_read_b128 v[136:139], v144 offset:1024
	ds_read_b128 v[140:143], v144 offset:2048
	ds_read_b128 v[144:147], v144 offset:3072
	ds_read_b128 v[148:151], v160
	ds_read_b128 v[152:155], v160 offset:1024
	ds_read_b128 v[156:159], v160 offset:2048
	ds_read_b128 v[160:163], v160 offset:3072
	v_lshl_add_u64 v[194:195], s[46:47], 0, v[172:173]
	s_add_i32 m0, s18, 0xc000
	ds_read_b128 v[176:179], v189
	ds_read_b128 v[190:193], v189 offset:1024
	ds_read_b128 v[198:201], v189 offset:2048
	ds_read_b128 v[202:205], v189 offset:3072
	ds_read_b128 v[206:209], v189 offset:4096
	ds_read_b128 v[210:213], v189 offset:5120
	ds_read_b128 v[214:217], v189 offset:6144
	ds_read_b128 v[218:221], v189 offset:7168
	global_load_lds_dwordx4 v[194:195], off
	v_lshl_add_u64 v[194:195], s[46:47], 0, v[174:175]
	s_add_i32 m0, s18, 0xe000
	s_nop 0
	global_load_lds_dwordx4 v[194:195], off
	s_waitcnt vmcnt(8)
	s_waitcnt lgkmcnt(0)
	s_barrier
	s_setprio 1
	s_waitcnt lgkmcnt(0)
	v_mfma_f32_16x16x32_bf16 v[126:129], v[132:135], v[176:179], v[126:129]
	v_mfma_f32_16x16x32_bf16 v[122:125], v[140:143], v[176:179], v[122:125]
	v_mfma_f32_16x16x32_bf16 v[114:117], v[132:135], v[198:201], v[114:117]
	v_mfma_f32_16x16x32_bf16 v[106:109], v[140:143], v[198:201], v[106:109]
	v_mfma_f32_16x16x32_bf16 v[98:101], v[132:135], v[206:209], v[98:101]
	v_mfma_f32_16x16x32_bf16 v[90:93], v[140:143], v[206:209], v[90:93]
	v_mfma_f32_16x16x32_bf16 v[82:85], v[132:135], v[214:217], v[82:85]
	v_mfma_f32_16x16x32_bf16 v[74:77], v[140:143], v[214:217], v[74:77]
	v_mfma_f32_16x16x32_bf16 v[126:129], v[136:139], v[190:193], v[126:129]
	v_mfma_f32_16x16x32_bf16 v[122:125], v[144:147], v[190:193], v[122:125]
	v_mfma_f32_16x16x32_bf16 v[114:117], v[136:139], v[202:205], v[114:117]
	v_mfma_f32_16x16x32_bf16 v[106:109], v[144:147], v[202:205], v[106:109]
	v_mfma_f32_16x16x32_bf16 v[98:101], v[136:139], v[210:213], v[98:101]
	v_mfma_f32_16x16x32_bf16 v[90:93], v[144:147], v[210:213], v[90:93]
	v_mfma_f32_16x16x32_bf16 v[82:85], v[136:139], v[218:221], v[82:85]
	v_mfma_f32_16x16x32_bf16 v[74:77], v[144:147], v[218:221], v[74:77]
	v_mfma_f32_16x16x32_bf16 v[118:121], v[148:151], v[176:179], v[118:121]
	v_mfma_f32_16x16x32_bf16 v[110:113], v[156:159], v[176:179], v[110:113]
	v_mfma_f32_16x16x32_bf16 v[102:105], v[148:151], v[198:201], v[102:105]
	v_mfma_f32_16x16x32_bf16 v[94:97], v[156:159], v[198:201], v[94:97]
	v_mfma_f32_16x16x32_bf16 v[86:89], v[148:151], v[206:209], v[86:89]
	v_mfma_f32_16x16x32_bf16 v[78:81], v[156:159], v[206:209], v[78:81]
	v_mfma_f32_16x16x32_bf16 v[70:73], v[148:151], v[214:217], v[70:73]
	v_mfma_f32_16x16x32_bf16 v[66:69], v[156:159], v[214:217], v[66:69]
	v_mfma_f32_16x16x32_bf16 v[118:121], v[152:155], v[190:193], v[118:121]
	v_mfma_f32_16x16x32_bf16 v[110:113], v[160:163], v[190:193], v[110:113]
	v_mfma_f32_16x16x32_bf16 v[102:105], v[152:155], v[202:205], v[102:105]
	v_mfma_f32_16x16x32_bf16 v[94:97], v[160:163], v[202:205], v[94:97]
	v_mfma_f32_16x16x32_bf16 v[86:89], v[152:155], v[210:213], v[86:89]
	v_mfma_f32_16x16x32_bf16 v[78:81], v[160:163], v[210:213], v[78:81]
	v_mfma_f32_16x16x32_bf16 v[70:73], v[152:155], v[218:221], v[70:73]
	v_mfma_f32_16x16x32_bf16 v[66:69], v[160:163], v[218:221], v[66:69]
	s_setprio 0
	s_barrier
	s_add_i32 s65, s65, s36
	v_lshl_add_u64 v[194:195], s[6:7], 0, v[166:167]
	s_mov_b32 m0, s65
	ds_read_b128 v[176:179], v189 offset:16384
	ds_read_b128 v[190:193], v189 offset:17408
	ds_read_b128 v[198:201], v189 offset:18432
	ds_read_b128 v[202:205], v189 offset:19456
	ds_read_b128 v[206:209], v189 offset:20480
	ds_read_b128 v[210:213], v189 offset:21504
	ds_read_b128 v[214:217], v189 offset:22528
	ds_read_b128 v[218:221], v189 offset:23552
	global_load_lds_dwordx4 v[194:195], off
	s_add_i32 m0, s65, 0x2000
	s_add_u32 s66, s6, 0x80000
	v_lshl_add_u64 v[222:223], s[6:7], 0, v[170:171]
	s_addc_u32 s67, s7, 0
	s_add_i32 s65, s68, s36
	global_load_lds_dwordx4 v[222:223], off
	v_lshl_add_u64 v[224:225], s[66:67], 0, v[166:167]
	s_mov_b32 m0, s65
	v_lshl_add_u64 v[226:227], s[48:49], 0, v[168:169]
	global_load_lds_dwordx4 v[224:225], off
	v_lshl_add_u64 v[224:225], s[66:67], 0, v[170:171]
	s_add_i32 m0, s65, 0x2000
	s_nop 0
	global_load_lds_dwordx4 v[224:225], off
	v_lshl_add_u64 v[224:225], s[48:49], 0, v[164:165]
	s_mov_b32 m0, s18
	s_nop 0
	global_load_lds_dwordx4 v[224:225], off
	s_mov_b32 m0, s31
	s_nop 0
	global_load_lds_dwordx4 v[226:227], off
	s_waitcnt vmcnt(8)
	s_waitcnt lgkmcnt(0)
	s_barrier
; #define PG8_STAGE(bufoff, gbase, voff) do { _Pragma("unroll") for (int _i = 0; _i < 2; ++_i) \
;         __builtin_amdgcn_global_load_lds((const unsigned*)((const char*)(gbase) + (voff)[_i]), (PG8_LAS unsigned*)(lds + (bufoff) + ldsw + _i * 8192), 16, 0, 0); } while (0)
; #define PG8_LDA(dst, b, h) do { _Pragma("unroll") for (int m = 0; m < 4; ++m) _Pragma("unroll") for (int k = 0; k < 2; ++k) dst[m][k] = *(const PG8_LAS bf16x8*)(lds + PG8_SA(b, h) + aoff + m * 2048 + k * 1024); } while (0)
; #define PG8_LDB(dst, b, h) do { _Pragma("unroll") for (int n = 0; n < 2; ++n) _Pragma("unroll") for (int k = 0; k < 2; ++k) dst[n][k] = *(const PG8_LAS bf16x8*)(lds + PG8_SB(b, h) + boff + n * 2048 + k * 1024); } while (0)
; #define PG8_MMA(ai, bj, At, Bt) do { __builtin_amdgcn_s_setprio(1); _Pragma("unroll") for (int m = 0; m < 4; ++m) _Pragma("unroll") for (int n = 0; n < 2; ++n) _Pragma("unroll") for (int k = 0; k < 2; ++k) \
;         acc[ai][bj][m][n] = __builtin_amdgcn_mfma_f32_16x16x32_bf16(Bt[n][k], At[m][k], acc[ai][bj][m][n], 0, 0, 0); __builtin_amdgcn_s_setprio(0); } while (0)
; #define PG8_WAIT_V(n) asm volatile("s_waitcnt vmcnt(" #n ")" ::: "memory")
; #define PG8_WAIT_L(n) asm volatile("s_waitcnt lgkmcnt(" #n ")" ::: "memory")
; #define PG8_BAR __builtin_amdgcn_s_barrier()
; #define PG8_SCHED __builtin_amdgcn_sched_barrier(0)
; #define PG8_STAGE(bufoff, gbase, voff) do { _Pragma("unroll") for (int _i = 0; _i < 2; ++_i) \
;         __builtin_amdgcn_global_load_lds((const unsigned*)((const char*)(gbase) + (voff)[_i]), (PG8_LAS unsigned*)(lds + (bufoff) + ldsw + _i * 8192), 16, 0, 0); } while (0)
; #define PG8_BAR __builtin_amdgcn_s_barrier()
; template <class Epi, class Sched, bool ALIGN_EPI = false, bool SP2 = false>
; __device__ __forceinline__ void gemm_phase(PG8_LAS unsigned char* lds, const Gemm g, const Sched& S, const Epi& E, const int tid) {
;     ...
;             PG8_WAIT_V(8); PG8_WAIT_L(0); PG8_BAR; PG8_MMA(1, 0, At, B0); PG8_MMA(1, 1, At, B1); PG8_BAR; PG8_SCHED;
;             PG8_LDB(B0, 1, 0); PG8_LDB(B1, 1, 1); PG8_SCHED; PG8_LDA(At, 1, 0); PG8_STAGE(PG8_SA(0, 1), a2 + hstep, voffA);
;             PG8_WAIT_V(8); PG8_WAIT_L(0); PG8_BAR; PG8_MMA(0, 0, At, B0); PG8_MMA(0, 1, At, B1); PG8_BAR; PG8_SCHED;
;             PG8_LDA(At, 1, 1); PG8_STAGE(PG8_SB(1, 0), b3, voffB); PG8_STAGE(PG8_SB(1, 1), b3 + hstep, voffB); PG8_STAGE(PG8_SA(1, 0), a3, voffA);
	s_setprio 1
	s_waitcnt lgkmcnt(0)
	v_mfma_f32_16x16x32_bf16 v[62:65], v[132:135], v[176:179], v[62:65]
	v_mfma_f32_16x16x32_bf16 v[58:61], v[140:143], v[176:179], v[58:61]
	v_mfma_f32_16x16x32_bf16 v[50:53], v[132:135], v[198:201], v[50:53]
	v_mfma_f32_16x16x32_bf16 v[42:45], v[140:143], v[198:201], v[42:45]
	v_mfma_f32_16x16x32_bf16 v[34:37], v[132:135], v[206:209], v[34:37]
	v_mfma_f32_16x16x32_bf16 v[26:29], v[140:143], v[206:209], v[26:29]
	v_mfma_f32_16x16x32_bf16 v[18:21], v[132:135], v[214:217], v[18:21]
	v_mfma_f32_16x16x32_bf16 v[10:13], v[140:143], v[214:217], v[10:13]
	v_mfma_f32_16x16x32_bf16 v[62:65], v[136:139], v[190:193], v[62:65]
	v_mfma_f32_16x16x32_bf16 v[58:61], v[144:147], v[190:193], v[58:61]
	v_mfma_f32_16x16x32_bf16 v[50:53], v[136:139], v[202:205], v[50:53]
	v_mfma_f32_16x16x32_bf16 v[42:45], v[144:147], v[202:205], v[42:45]
	v_mfma_f32_16x16x32_bf16 v[34:37], v[136:139], v[210:213], v[34:37]
	v_mfma_f32_16x16x32_bf16 v[26:29], v[144:147], v[210:213], v[26:29]
	v_mfma_f32_16x16x32_bf16 v[18:21], v[136:139], v[218:221], v[18:21]
	v_mfma_f32_16x16x32_bf16 v[10:13], v[144:147], v[218:221], v[10:13]
	v_mfma_f32_16x16x32_bf16 v[54:57], v[148:151], v[176:179], v[54:57]
	v_mfma_f32_16x16x32_bf16 v[46:49], v[156:159], v[176:179], v[46:49]
	v_mfma_f32_16x16x32_bf16 v[38:41], v[148:151], v[198:201], v[38:41]
	v_mfma_f32_16x16x32_bf16 v[30:33], v[156:159], v[198:201], v[30:33]
	v_mfma_f32_16x16x32_bf16 v[22:25], v[148:151], v[206:209], v[22:25]
	v_mfma_f32_16x16x32_bf16 v[14:17], v[156:159], v[206:209], v[14:17]
	v_mfma_f32_16x16x32_bf16 v[6:9], v[148:151], v[214:217], v[6:9]
	v_mfma_f32_16x16x32_bf16 v[2:5], v[156:159], v[214:217], v[2:5]
	v_mfma_f32_16x16x32_bf16 v[54:57], v[152:155], v[190:193], v[54:57]
	v_mfma_f32_16x16x32_bf16 v[46:49], v[160:163], v[190:193], v[46:49]
	v_mfma_f32_16x16x32_bf16 v[38:41], v[152:155], v[202:205], v[38:41]
	v_mfma_f32_16x16x32_bf16 v[30:33], v[160:163], v[202:205], v[30:33]
	v_mfma_f32_16x16x32_bf16 v[22:25], v[152:155], v[210:213], v[22:25]
	v_mfma_f32_16x16x32_bf16 v[14:17], v[160:163], v[210:213], v[14:17]
	v_mfma_f32_16x16x32_bf16 v[6:9], v[152:155], v[218:221], v[6:9]
	v_mfma_f32_16x16x32_bf16 v[2:5], v[160:163], v[218:221], v[2:5]
	s_setprio 0
	s_barrier
	s_add_i32 s65, 0, 0x18000
	s_add_i32 s66, 0, 0x1c000
	v_add_u32_e32 v144, s65, v180
	v_add_u32_e32 v160, s66, v180
	ds_read_b128 v[132:135], v144
	ds_read_b128 v[136:139], v144 offset:1024
	ds_read_b128 v[140:143], v144 offset:2048
	ds_read_b128 v[144:147], v144 offset:3072
	ds_read_b128 v[148:151], v160
	ds_read_b128 v[152:155], v160 offset:1024
	ds_read_b128 v[156:159], v160 offset:2048
	ds_read_b128 v[160:163], v160 offset:3072
	s_add_u32 s48, s48, 0x80000
	s_addc_u32 s49, s49, 0
	s_mov_b32 m0, s37
	v_lshl_add_u64 v[228:229], s[48:49], 0, v[164:165]
	ds_read_b128 v[176:179], v189 offset:32768
	ds_read_b128 v[190:193], v189 offset:33792
	ds_read_b128 v[198:201], v189 offset:34816
	ds_read_b128 v[202:205], v189 offset:35840
	ds_read_b128 v[206:209], v189 offset:36864
	ds_read_b128 v[210:213], v189 offset:37888
	ds_read_b128 v[214:217], v189 offset:38912
	ds_read_b128 v[218:221], v189 offset:39936
	global_load_lds_dwordx4 v[228:229], off
	v_lshl_add_u64 v[228:229], s[48:49], 0, v[168:169]
	s_mov_b32 m0, s50
	s_nop 0
	global_load_lds_dwordx4 v[228:229], off
	s_waitcnt vmcnt(8)
	s_waitcnt lgkmcnt(0)
	s_barrier
	s_setprio 1
	s_waitcnt lgkmcnt(0)
	v_mfma_f32_16x16x32_bf16 v[126:129], v[132:135], v[176:179], v[126:129]
	v_mfma_f32_16x16x32_bf16 v[122:125], v[140:143], v[176:179], v[122:125]
	v_mfma_f32_16x16x32_bf16 v[114:117], v[132:135], v[198:201], v[114:117]
	v_mfma_f32_16x16x32_bf16 v[106:109], v[140:143], v[198:201], v[106:109]
	v_mfma_f32_16x16x32_bf16 v[98:101], v[132:135], v[206:209], v[98:101]
	v_mfma_f32_16x16x32_bf16 v[90:93], v[140:143], v[206:209], v[90:93]
	v_mfma_f32_16x16x32_bf16 v[82:85], v[132:135], v[214:217], v[82:85]
	v_mfma_f32_16x16x32_bf16 v[74:77], v[140:143], v[214:217], v[74:77]
	v_mfma_f32_16x16x32_bf16 v[126:129], v[136:139], v[190:193], v[126:129]
	v_mfma_f32_16x16x32_bf16 v[122:125], v[144:147], v[190:193], v[122:125]
	v_mfma_f32_16x16x32_bf16 v[114:117], v[136:139], v[202:205], v[114:117]
	v_mfma_f32_16x16x32_bf16 v[106:109], v[144:147], v[202:205], v[106:109]
	v_mfma_f32_16x16x32_bf16 v[98:101], v[136:139], v[210:213], v[98:101]
	v_mfma_f32_16x16x32_bf16 v[90:93], v[144:147], v[210:213], v[90:93]
	v_mfma_f32_16x16x32_bf16 v[82:85], v[136:139], v[218:221], v[82:85]
	v_mfma_f32_16x16x32_bf16 v[74:77], v[144:147], v[218:221], v[74:77]
	v_mfma_f32_16x16x32_bf16 v[118:121], v[148:151], v[176:179], v[118:121]
	v_mfma_f32_16x16x32_bf16 v[110:113], v[156:159], v[176:179], v[110:113]
	v_mfma_f32_16x16x32_bf16 v[102:105], v[148:151], v[198:201], v[102:105]
	v_mfma_f32_16x16x32_bf16 v[94:97], v[156:159], v[198:201], v[94:97]
	v_mfma_f32_16x16x32_bf16 v[86:89], v[148:151], v[206:209], v[86:89]
	v_mfma_f32_16x16x32_bf16 v[78:81], v[156:159], v[206:209], v[78:81]
	v_mfma_f32_16x16x32_bf16 v[70:73], v[148:151], v[214:217], v[70:73]
	v_mfma_f32_16x16x32_bf16 v[66:69], v[156:159], v[214:217], v[66:69]
	v_mfma_f32_16x16x32_bf16 v[118:121], v[152:155], v[190:193], v[118:121]
	v_mfma_f32_16x16x32_bf16 v[110:113], v[160:163], v[190:193], v[110:113]
	v_mfma_f32_16x16x32_bf16 v[102:105], v[152:155], v[202:205], v[102:105]
	v_mfma_f32_16x16x32_bf16 v[94:97], v[160:163], v[202:205], v[94:97]
	v_mfma_f32_16x16x32_bf16 v[86:89], v[152:155], v[210:213], v[86:89]
	v_mfma_f32_16x16x32_bf16 v[78:81], v[160:163], v[210:213], v[78:81]
	v_mfma_f32_16x16x32_bf16 v[70:73], v[152:155], v[218:221], v[70:73]
	v_mfma_f32_16x16x32_bf16 v[66:69], v[160:163], v[218:221], v[66:69]
	s_setprio 0
	s_barrier
; #define PG8_STAGE(bufoff, gbase, voff) do { _Pragma("unroll") for (int _i = 0; _i < 2; ++_i) \
;         __builtin_amdgcn_global_load_lds((const unsigned*)((const char*)(gbase) + (voff)[_i]), (PG8_LAS unsigned*)(lds + (bufoff) + ldsw + _i * 8192), 16, 0, 0); } while (0)
; #define PG8_LDA(dst, b, h) do { _Pragma("unroll") for (int m = 0; m < 4; ++m) _Pragma("unroll") for (int k = 0; k < 2; ++k) dst[m][k] = *(const PG8_LAS bf16x8*)(lds + PG8_SA(b, h) + aoff + m * 2048 + k * 1024); } while (0)
; #define PG8_MMA(ai, bj, At, Bt) do { __builtin_amdgcn_s_setprio(1); _Pragma("unroll") for (int m = 0; m < 4; ++m) _Pragma("unroll") for (int n = 0; n < 2; ++n) _Pragma("unroll") for (int k = 0; k < 2; ++k) \
;         acc[ai][bj][m][n] = __builtin_amdgcn_mfma_f32_16x16x32_bf16(Bt[n][k], At[m][k], acc[ai][bj][m][n], 0, 0, 0); __builtin_amdgcn_s_setprio(0); } while (0)
; #define PG8_WAIT_V(n) asm volatile("s_waitcnt vmcnt(" #n ")" ::: "memory")
; #define PG8_WAIT_L(n) asm volatile("s_waitcnt lgkmcnt(" #n ")" ::: "memory")
; #define PG8_BAR __builtin_amdgcn_s_barrier()
; #define PG8_SCHED __builtin_amdgcn_sched_barrier(0)
; #define PG8_STAGE(bufoff, gbase, voff) do { _Pragma("unroll") for (int _i = 0; _i < 2; ++_i) \
;         __builtin_amdgcn_global_load_lds((const unsigned*)((const char*)(gbase) + (voff)[_i]), (PG8_LAS unsigned*)(lds + (bufoff) + ldsw + _i * 8192), 16, 0, 0); } while (0)
; #define PG8_LDA(dst, b, h) do { _Pragma("unroll") for (int mb = 0; mb < 2; ++mb) _Pragma("unroll") for (int s = 0; s < 2; ++s) \
;         dst[mb][s] = cat8(*(const PG8_LAS bf16x8*)(lds + PG8_SA(b, h) + aoffk[s][0] + mb * 4096), *(const PG8_LAS bf16x8*)(lds + PG8_SA(b, h) + aoffk[s][1] + mb * 4096)); } while (0)
; template <class Epi, class Sched, bool ALIGN_EPI = false, bool SP2 = false>
; __device__ __forceinline__ void gemm_phase(PG8_LAS unsigned char* lds, const Gemm g, const Sched& S, const Epi& E, const int tid) {
;     ...
;         for (int t = 0; t < nt; t += 2) {
;     ...
;             PG8_WAIT_V(8); PG8_WAIT_L(0); PG8_BAR; PG8_MMA(0, 0, At, B0); PG8_MMA(0, 1, At, B1); PG8_BAR; PG8_SCHED;
;             PG8_LDA(At, 1, 1); PG8_STAGE(PG8_SB(1, 0), b3, voffB); PG8_STAGE(PG8_SB(1, 1), b3 + hstep, voffB); PG8_STAGE(PG8_SA(1, 0), a3, voffA);
;             PG8_WAIT_V(8); PG8_WAIT_L(0); PG8_BAR; PG8_MMA(1, 0, At, B0); PG8_MMA(1, 1, At, B1); PG8_BAR; PG8_SCHED;
	s_add_i32 s48, s65, s36
	v_lshl_add_u64 v[194:195], v[194:195], 0, s[34:35]
	s_mov_b32 m0, s48
	ds_read_b128 v[176:179], v189 offset:49152
	ds_read_b128 v[190:193], v189 offset:50176
	ds_read_b128 v[198:201], v189 offset:51200
	ds_read_b128 v[202:205], v189 offset:52224
	ds_read_b128 v[206:209], v189 offset:53248
	ds_read_b128 v[210:213], v189 offset:54272
	ds_read_b128 v[214:217], v189 offset:55296
	ds_read_b128 v[218:221], v189 offset:56320
	global_load_lds_dwordx4 v[194:195], off
	s_add_i32 m0, s48, 0x2000
	s_add_u32 s6, s6, 0x80080
	v_lshl_add_u64 v[194:195], v[222:223], 0, s[34:35]
	s_addc_u32 s7, s7, 0
	s_add_i32 s48, s66, s36
	global_load_lds_dwordx4 v[194:195], off
	v_lshl_add_u64 v[194:195], s[6:7], 0, v[166:167]
	s_mov_b32 m0, s48
	s_nop 0
	global_load_lds_dwordx4 v[194:195], off
	v_lshl_add_u64 v[194:195], s[6:7], 0, v[170:171]
	s_add_i32 m0, s48, 0x2000
	s_nop 0
	global_load_lds_dwordx4 v[194:195], off
	v_lshl_add_u64 v[194:195], v[224:225], 0, s[34:35]
	s_mov_b32 m0, s26
	s_nop 0
	global_load_lds_dwordx4 v[194:195], off
	v_lshl_add_u64 v[194:195], v[226:227], 0, s[34:35]
	s_mov_b32 m0, s52
	s_nop 0
	global_load_lds_dwordx4 v[194:195], off
	s_waitcnt vmcnt(8)
	s_waitcnt lgkmcnt(0)
	s_barrier
	s_setprio 1
	s_waitcnt lgkmcnt(0)
	v_mfma_f32_16x16x32_bf16 v[62:65], v[132:135], v[176:179], v[62:65]
	v_mfma_f32_16x16x32_bf16 v[58:61], v[140:143], v[176:179], v[58:61]
	v_mfma_f32_16x16x32_bf16 v[50:53], v[132:135], v[198:201], v[50:53]
	v_mfma_f32_16x16x32_bf16 v[42:45], v[140:143], v[198:201], v[42:45]
	v_mfma_f32_16x16x32_bf16 v[34:37], v[132:135], v[206:209], v[34:37]
	v_mfma_f32_16x16x32_bf16 v[26:29], v[140:143], v[206:209], v[26:29]
	v_mfma_f32_16x16x32_bf16 v[18:21], v[132:135], v[214:217], v[18:21]
	v_mfma_f32_16x16x32_bf16 v[10:13], v[140:143], v[214:217], v[10:13]
	v_mfma_f32_16x16x32_bf16 v[62:65], v[136:139], v[190:193], v[62:65]
	v_mfma_f32_16x16x32_bf16 v[58:61], v[144:147], v[190:193], v[58:61]
	v_mfma_f32_16x16x32_bf16 v[50:53], v[136:139], v[202:205], v[50:53]
	v_mfma_f32_16x16x32_bf16 v[42:45], v[144:147], v[202:205], v[42:45]
	v_mfma_f32_16x16x32_bf16 v[34:37], v[136:139], v[210:213], v[34:37]
	v_mfma_f32_16x16x32_bf16 v[26:29], v[144:147], v[210:213], v[26:29]
	v_mfma_f32_16x16x32_bf16 v[18:21], v[136:139], v[218:221], v[18:21]
	v_mfma_f32_16x16x32_bf16 v[10:13], v[144:147], v[218:221], v[10:13]
	v_mfma_f32_16x16x32_bf16 v[54:57], v[148:151], v[176:179], v[54:57]
	v_mfma_f32_16x16x32_bf16 v[46:49], v[156:159], v[176:179], v[46:49]
	v_mfma_f32_16x16x32_bf16 v[38:41], v[148:151], v[198:201], v[38:41]
	v_mfma_f32_16x16x32_bf16 v[30:33], v[156:159], v[198:201], v[30:33]
	v_mfma_f32_16x16x32_bf16 v[22:25], v[148:151], v[206:209], v[22:25]
	v_mfma_f32_16x16x32_bf16 v[14:17], v[156:159], v[206:209], v[14:17]
	v_mfma_f32_16x16x32_bf16 v[6:9], v[148:151], v[214:217], v[6:9]
	v_mfma_f32_16x16x32_bf16 v[2:5], v[156:159], v[214:217], v[2:5]
	v_mfma_f32_16x16x32_bf16 v[54:57], v[152:155], v[190:193], v[54:57]
	v_mfma_f32_16x16x32_bf16 v[46:49], v[160:163], v[190:193], v[46:49]
	v_mfma_f32_16x16x32_bf16 v[38:41], v[152:155], v[202:205], v[38:41]
	v_mfma_f32_16x16x32_bf16 v[30:33], v[160:163], v[202:205], v[30:33]
	v_mfma_f32_16x16x32_bf16 v[22:25], v[152:155], v[210:213], v[22:25]
	v_mfma_f32_16x16x32_bf16 v[14:17], v[160:163], v[210:213], v[14:17]
	v_mfma_f32_16x16x32_bf16 v[6:9], v[152:155], v[218:221], v[6:9]
	v_mfma_f32_16x16x32_bf16 v[2:5], v[160:163], v[218:221], v[2:5]
	s_setprio 0
	s_barrier
	s_add_u32 s46, s46, 0x100
	s_addc_u32 s47, s47, 0
	s_add_u32 s39, s39, 0x100
	s_addc_u32 s45, s45, 0
	s_cmp_ge_i32 s63, s64
	s_mov_b32 s6, s63
	s_cbranch_scc0 .LBB0_1589
	s_and_b64 vcc, exec, s[4:5]
	s_cbranch_vccz .LBB0_1592
	s_barrier

; #define PG8_STAGE(bufoff, gbase, voff) do { _Pragma("unroll") for (int _i = 0; _i < 2; ++_i) \
;         __builtin_amdgcn_global_load_lds((const unsigned*)((const char*)(gbase) + (voff)[_i]), (PG8_LAS unsigned*)(lds + (bufoff) + ldsw + _i * 8192), 16, 0, 0); } while (0)
; #define PG8_LDA(dst, b, h) do { _Pragma("unroll") for (int m = 0; m < 4; ++m) _Pragma("unroll") for (int k = 0; k < 2; ++k) dst[m][k] = *(const PG8_LAS bf16x8*)(lds + PG8_SA(b, h) + aoff + m * 2048 + k * 1024); } while (0)
; #define PG8_LDB(dst, b, h) do { _Pragma("unroll") for (int n = 0; n < 2; ++n) _Pragma("unroll") for (int k = 0; k < 2; ++k) dst[n][k] = *(const PG8_LAS bf16x8*)(lds + PG8_SB(b, h) + boff + n * 2048 + k * 1024); } while (0)
; #define PG8_WAIT_V(n) asm volatile("s_waitcnt vmcnt(" #n ")" ::: "memory")
; #define PG8_WAIT_L(n) asm volatile("s_waitcnt lgkmcnt(" #n ")" ::: "memory")
; #define PG8_BAR __builtin_amdgcn_s_barrier()
; #define PG8_SCHED __builtin_amdgcn_sched_barrier(0)
; #define PG8_WAIT_V(n) asm volatile("s_waitcnt vmcnt(" #n ")" ::: "memory")
; template <class Epi, class Sched, int SCW, int SCX, int SCW1 = SCW>
; __device__ __forceinline__ void gemm_phase_f8(PG8_LAS unsigned char* lds, const Gemm g, const Sched& S, const Epi& E, const int tid) {
;     ...
;         const char* nA = has_next ? (const char*)g.A + (size_t)nxt.pm * tstep + (size_t)nxt.k0 : cA; const char* nB = has_next ? (const char*)g.Bt + (size_t)nxt.pn * tstep + (size_t)nxt.k0 * 256 : cB;
;         for (int t = 0; t < nt; t += 2) {
;             const bool last = (t == nt - 2);
;             const char* a1 = cA + (size_t)(t + 1) * kstep;
;             const char* a2 = last ? nA : cA + (size_t)(t + 2) * kstep; const char* b2 = last ? nB : cB + (size_t)(t + 2) * kstepB;
;             const char* a3 = a2 + kstep; const char* b3 = b2 + kstepB;
;             if (last && has_next) S.a_ready(nxt);
;             PG8_LDB(B0, 0, 0); PG8_LDB(B1, 0, 1); PG8_SCHED; PG8_LDA(At, 0, 0); PG8_STAGE(PG8_SA(1, 1), a1 + hstep, voffA);
;             PG8_WAIT_V(8); PG8_WAIT_L(0); PG8_BAR; PG8_MMA(0, 0, At, B0); PG8_MMA(0, 1, At, B1); PG8_BAR; PG8_SCHED;
;             PG8_LDA(At, 0, 1); PG8_STAGE(PG8_SB(0, 0), b2, voffB); PG8_STAGE(PG8_SB(0, 1), b2 + hstepB, voffB); PG8_STAGE(PG8_SA(0, 0), a2, voffA);
;             PG8_WAIT_V(8); PG8_WAIT_L(0); PG8_BAR; PG8_MMA(1, 0, At, B0); PG8_MMA(1, 1, At, B1); PG8_BAR; PG8_SCHED;
.LBB0_1896:
	s_add_u32 s6, s40, 0xfffc0080
	s_addc_u32 s7, s41, -1
	s_add_i32 s67, 0, 0x10000
	s_cmp_eq_u32 s66, 12
	v_add_u32_e32 v144, s67, v131
	s_cselect_b32 s43, s15, s7
	s_cselect_b32 s42, s63, s6
	v_add_u32_e32 v145, s67, v150
	ds_read_b128 v[160:163], v144
	ds_read_b128 v[164:167], v145
	v_add_u32_e32 v144, s67, v151
	s_cselect_b32 s7, s17, s65
	s_cselect_b32 s6, s21, s64
	s_add_i32 s70, 0, 0x14000
	v_add_u32_e32 v145, s67, v152
	ds_read_b128 v[168:171], v144
	ds_read_b128 v[172:175], v145
	v_add_u32_e32 v144, s70, v131
	v_add_u32_e32 v145, s70, v150
	ds_read_b128 v[176:179], v144
	ds_read_b128 v[180:183], v145
	v_add_u32_e32 v144, s70, v151
	v_add_u32_e32 v145, s70, v152
	ds_read_b128 v[184:187], v144
	ds_read_b128 v[188:191], v145
	v_lshl_add_u64 v[144:145], s[40:41], 0, v[140:141]
	s_add_i32 m0, s31, 0xc000
	ds_read_b128 v[198:201], v155
	ds_read_b128 v[206:209], v155 offset:4096
	ds_read_b128 v[202:205], v156
	ds_read_b128 v[210:213], v156 offset:4096
	ds_read_b128 v[214:217], v157
	ds_read_b128 v[222:225], v157 offset:4096
	ds_read_b128 v[218:221], v158
	ds_read_b128 v[226:229], v158 offset:4096
	global_load_lds_dwordx4 v[144:145], off
	v_lshl_add_u64 v[144:145], s[40:41], 0, v[142:143]
	s_add_i32 m0, s31, 0xe000
	s_nop 0
	global_load_lds_dwordx4 v[144:145], off
	s_waitcnt vmcnt(8)
	s_waitcnt lgkmcnt(0)
	s_barrier
	s_setprio 1
	s_waitcnt lgkmcnt(0)
	v_mfma_scale_f32_32x32x64_f8f6f4 v[98:113], v[160:167], v[198:205], v[98:113], v233, v232 op_sel_hi:[0,0,0]
	v_mfma_scale_f32_32x32x64_f8f6f4 v[66:81], v[160:167], v[206:213], v[66:81], v233, v232 op_sel_hi:[0,0,0]
	v_mfma_scale_f32_32x32x64_f8f6f4 v[98:113], v[168:175], v[214:221], v[98:113], v233, v232 op_sel_hi:[0,0,0]
	v_mfma_scale_f32_32x32x64_f8f6f4 v[66:81], v[168:175], v[222:229], v[66:81], v233, v232 op_sel_hi:[0,0,0]
	v_mfma_scale_f32_32x32x64_f8f6f4 v[114:129], v[176:183], v[198:205], v[114:129], v232, v232 op_sel_hi:[0,0,0]
	v_mfma_scale_f32_32x32x64_f8f6f4 v[82:97], v[176:183], v[206:213], v[82:97], v232, v232 op_sel_hi:[0,0,0]
	v_mfma_scale_f32_32x32x64_f8f6f4 v[114:129], v[184:191], v[214:221], v[114:129], v232, v232 op_sel_hi:[0,0,0]
	v_mfma_scale_f32_32x32x64_f8f6f4 v[82:97], v[184:191], v[222:229], v[82:97], v232, v232 op_sel_hi:[0,0,0]
	s_setprio 0
	s_barrier
	s_add_i32 s67, s67, s48
	v_lshl_add_u64 v[144:145], s[6:7], 0, v[136:137]
	s_mov_b32 m0, s67
	ds_read_b128 v[198:201], v155 offset:16384
	ds_read_b128 v[206:209], v155 offset:20480
	ds_read_b128 v[202:205], v156 offset:16384
	ds_read_b128 v[210:213], v156 offset:20480
	ds_read_b128 v[214:217], v157 offset:16384
	ds_read_b128 v[222:225], v157 offset:20480
	ds_read_b128 v[218:221], v158 offset:16384
	ds_read_b128 v[226:229], v158 offset:20480
	global_load_lds_dwordx4 v[144:145], off
	s_add_i32 m0, s67, 0x2000
	s_add_u32 s68, s6, 0x4000
	v_lshl_add_u64 v[144:145], s[6:7], 0, v[132:133]
	s_addc_u32 s69, s7, 0
	s_add_i32 s67, s70, s48
	global_load_lds_dwordx4 v[144:145], off
	v_lshl_add_u64 v[144:145], s[68:69], 0, v[136:137]
	s_mov_b32 m0, s67
	v_lshl_add_u64 v[146:147], s[42:43], 0, v[134:135]
	global_load_lds_dwordx4 v[144:145], off
	v_lshl_add_u64 v[144:145], s[68:69], 0, v[132:133]
	s_add_i32 m0, s67, 0x2000
	s_nop 0
	global_load_lds_dwordx4 v[144:145], off
	v_lshl_add_u64 v[144:145], s[42:43], 0, v[138:139]
	s_mov_b32 m0, s31
	s_nop 0
	global_load_lds_dwordx4 v[144:145], off
	s_mov_b32 m0, s39
	s_nop 0
	global_load_lds_dwordx4 v[146:147], off
	s_waitcnt vmcnt(8)
	s_waitcnt lgkmcnt(0)
	s_barrier
	s_setprio 1
	s_waitcnt lgkmcnt(0)
	v_mfma_scale_f32_32x32x64_f8f6f4 v[34:49], v[160:167], v[198:205], v[34:49], v233, v232 op_sel_hi:[0,0,0]
	v_mfma_scale_f32_32x32x64_f8f6f4 v[2:17], v[160:167], v[206:213], v[2:17], v233, v232 op_sel_hi:[0,0,0]
	v_mfma_scale_f32_32x32x64_f8f6f4 v[34:49], v[168:175], v[214:221], v[34:49], v233, v232 op_sel_hi:[0,0,0]
	v_mfma_scale_f32_32x32x64_f8f6f4 v[2:17], v[168:175], v[222:229], v[2:17], v233, v232 op_sel_hi:[0,0,0]
	v_mfma_scale_f32_32x32x64_f8f6f4 v[50:65], v[176:183], v[198:205], v[50:65], v232, v232 op_sel_hi:[0,0,0]
	v_mfma_scale_f32_32x32x64_f8f6f4 v[18:33], v[176:183], v[206:213], v[18:33], v232, v232 op_sel_hi:[0,0,0]
	v_mfma_scale_f32_32x32x64_f8f6f4 v[50:65], v[184:191], v[214:221], v[50:65], v232, v232 op_sel_hi:[0,0,0]
	v_mfma_scale_f32_32x32x64_f8f6f4 v[18:33], v[184:191], v[222:229], v[18:33], v232, v232 op_sel_hi:[0,0,0]
	s_setprio 0
	s_barrier
; #define PG8_STAGE(bufoff, gbase, voff) do { _Pragma("unroll") for (int _i = 0; _i < 2; ++_i) \
;         __builtin_amdgcn_global_load_lds((const unsigned*)((const char*)(gbase) + (voff)[_i]), (PG8_LAS unsigned*)(lds + (bufoff) + ldsw + _i * 8192), 16, 0, 0); } while (0)
; #define PG8_LDA(dst, b, h) do { _Pragma("unroll") for (int m = 0; m < 4; ++m) _Pragma("unroll") for (int k = 0; k < 2; ++k) dst[m][k] = *(const PG8_LAS bf16x8*)(lds + PG8_SA(b, h) + aoff + m * 2048 + k * 1024); } while (0)
; #define PG8_LDB(dst, b, h) do { _Pragma("unroll") for (int n = 0; n < 2; ++n) _Pragma("unroll") for (int k = 0; k < 2; ++k) dst[n][k] = *(const PG8_LAS bf16x8*)(lds + PG8_SB(b, h) + boff + n * 2048 + k * 1024); } while (0)
; #define PG8_MMA(ai, bj, At, Bt) do { __builtin_amdgcn_s_setprio(1); _Pragma("unroll") for (int m = 0; m < 4; ++m) _Pragma("unroll") for (int n = 0; n < 2; ++n) _Pragma("unroll") for (int k = 0; k < 2; ++k) \
;         acc[ai][bj][m][n] = __builtin_amdgcn_mfma_f32_16x16x32_bf16(Bt[n][k], At[m][k], acc[ai][bj][m][n], 0, 0, 0); __builtin_amdgcn_s_setprio(0); } while (0)
; #define PG8_WAIT_V(n) asm volatile("s_waitcnt vmcnt(" #n ")" ::: "memory")
; #define PG8_WAIT_L(n) asm volatile("s_waitcnt lgkmcnt(" #n ")" ::: "memory")
; #define PG8_BAR __builtin_amdgcn_s_barrier()
; #define PG8_SCHED __builtin_amdgcn_sched_barrier(0)
; #define PG8_STAGE(bufoff, gbase, voff) do { _Pragma("unroll") for (int _i = 0; _i < 2; ++_i) \
;         __builtin_amdgcn_global_load_lds((const unsigned*)((const char*)(gbase) + (voff)[_i]), (PG8_LAS unsigned*)(lds + (bufoff) + ldsw + _i * 8192), 16, 0, 0); } while (0)
; template <class Epi, class Sched, int SCW, int SCX, int SCW1 = SCW>
; __device__ __forceinline__ void gemm_phase_f8(PG8_LAS unsigned char* lds, const Gemm g, const Sched& S, const Epi& E, const int tid) {
;     ...
;             PG8_LDB(B0, 1, 0); PG8_LDB(B1, 1, 1); PG8_SCHED; PG8_LDA(At, 1, 0); PG8_STAGE(PG8_SA(0, 1), a2 + hstep, voffA);
;             PG8_WAIT_V(8); PG8_WAIT_L(0); PG8_BAR; PG8_MMA(0, 0, At, B0); PG8_MMA(0, 1, At, B1); PG8_BAR; PG8_SCHED;
;             PG8_LDA(At, 1, 1); PG8_STAGE(PG8_SB(1, 0), b3, voffB); PG8_STAGE(PG8_SB(1, 1), b3 + hstepB, voffB); PG8_STAGE(PG8_SA(1, 0), a3, voffA);
;             PG8_WAIT_V(8); PG8_WAIT_L(0); PG8_BAR; PG8_MMA(1, 0, At, B0); PG8_MMA(1, 1, At, B1); PG8_BAR; PG8_SCHED;
;         }
	s_add_i32 s67, 0, 0x18000
	v_add_u32_e32 v148, s67, v131
	v_add_u32_e32 v149, s67, v150
	ds_read_b128 v[160:163], v148
	ds_read_b128 v[164:167], v149
	v_add_u32_e32 v148, s67, v151
	s_add_i32 s68, 0, 0x1c000
	v_add_u32_e32 v149, s67, v152
	ds_read_b128 v[168:171], v148
	ds_read_b128 v[172:175], v149
	v_add_u32_e32 v148, s68, v131
	v_add_u32_e32 v149, s68, v150
	ds_read_b128 v[176:179], v148
	ds_read_b128 v[180:183], v149
	v_add_u32_e32 v148, s68, v151
	v_add_u32_e32 v149, s68, v152
	ds_read_b128 v[184:187], v148
	ds_read_b128 v[188:191], v149
	s_add_u32 s42, s42, 0x40000
	s_addc_u32 s43, s43, 0
	s_mov_b32 m0, s57
	v_lshl_add_u64 v[148:149], s[42:43], 0, v[138:139]
	ds_read_b128 v[198:201], v155 offset:32768
	ds_read_b128 v[206:209], v155 offset:36864
	ds_read_b128 v[202:205], v156 offset:32768
	ds_read_b128 v[210:213], v156 offset:36864
	ds_read_b128 v[214:217], v157 offset:32768
	ds_read_b128 v[222:225], v157 offset:36864
	ds_read_b128 v[218:221], v158 offset:32768
	ds_read_b128 v[226:229], v158 offset:36864
	global_load_lds_dwordx4 v[148:149], off
	v_lshl_add_u64 v[148:149], s[42:43], 0, v[134:135]
	s_mov_b32 m0, s58
	s_nop 0
	global_load_lds_dwordx4 v[148:149], off
	s_waitcnt vmcnt(8)
	s_waitcnt lgkmcnt(0)
	s_barrier
	s_setprio 1
	s_waitcnt lgkmcnt(0)
	v_mfma_scale_f32_32x32x64_f8f6f4 v[98:113], v[160:167], v[198:205], v[98:113], v233, v232 op_sel_hi:[0,0,0]
	v_mfma_scale_f32_32x32x64_f8f6f4 v[66:81], v[160:167], v[206:213], v[66:81], v233, v232 op_sel_hi:[0,0,0]
	v_mfma_scale_f32_32x32x64_f8f6f4 v[98:113], v[168:175], v[214:221], v[98:113], v233, v232 op_sel_hi:[0,0,0]
	v_mfma_scale_f32_32x32x64_f8f6f4 v[66:81], v[168:175], v[222:229], v[66:81], v233, v232 op_sel_hi:[0,0,0]
	v_mfma_scale_f32_32x32x64_f8f6f4 v[114:129], v[176:183], v[198:205], v[114:129], v232, v232 op_sel_hi:[0,0,0]
	v_mfma_scale_f32_32x32x64_f8f6f4 v[82:97], v[176:183], v[206:213], v[82:97], v232, v232 op_sel_hi:[0,0,0]
	v_mfma_scale_f32_32x32x64_f8f6f4 v[114:129], v[184:191], v[214:221], v[114:129], v232, v232 op_sel_hi:[0,0,0]
	v_mfma_scale_f32_32x32x64_f8f6f4 v[82:97], v[184:191], v[222:229], v[82:97], v232, v232 op_sel_hi:[0,0,0]
	s_setprio 0
	s_barrier
	s_add_u32 s42, s6, 0x8000
	s_addc_u32 s43, s7, 0
	s_add_i32 s67, s67, s48
	v_lshl_add_u64 v[148:149], s[42:43], 0, v[136:137]
	s_mov_b32 m0, s67
	ds_read_b128 v[198:201], v155 offset:49152
	ds_read_b128 v[206:209], v155 offset:53248
	ds_read_b128 v[202:205], v156 offset:49152
	ds_read_b128 v[210:213], v156 offset:53248
	ds_read_b128 v[214:217], v157 offset:49152
	ds_read_b128 v[222:225], v157 offset:53248
	ds_read_b128 v[218:221], v158 offset:49152
	ds_read_b128 v[226:229], v158 offset:53248
	global_load_lds_dwordx4 v[148:149], off
	s_add_i32 m0, s67, 0x2000
	s_add_u32 s6, s6, 0xc000
	v_lshl_add_u64 v[148:149], s[42:43], 0, v[132:133]
	s_addc_u32 s7, s7, 0
	s_add_i32 s42, s68, s48
	global_load_lds_dwordx4 v[148:149], off
	v_lshl_add_u64 v[148:149], s[6:7], 0, v[136:137]
	s_mov_b32 m0, s42
	v_lshl_add_u64 v[144:145], v[144:145], 0, s[34:35]
	global_load_lds_dwordx4 v[148:149], off
	v_lshl_add_u64 v[148:149], s[6:7], 0, v[132:133]
	s_add_i32 m0, s42, 0x2000
	s_nop 0
	global_load_lds_dwordx4 v[148:149], off
	s_mov_b32 m0, s59
	s_nop 0
	global_load_lds_dwordx4 v[144:145], off
	v_lshl_add_u64 v[144:145], v[146:147], 0, s[34:35]
	s_mov_b32 m0, s60
	s_nop 0
	global_load_lds_dwordx4 v[144:145], off
	s_waitcnt vmcnt(8)
	s_waitcnt lgkmcnt(0)
	s_barrier
	s_setprio 1
	s_waitcnt lgkmcnt(0)
	v_mfma_scale_f32_32x32x64_f8f6f4 v[34:49], v[160:167], v[198:205], v[34:49], v233, v232 op_sel_hi:[0,0,0]
	v_mfma_scale_f32_32x32x64_f8f6f4 v[2:17], v[160:167], v[206:213], v[2:17], v233, v232 op_sel_hi:[0,0,0]
	v_mfma_scale_f32_32x32x64_f8f6f4 v[34:49], v[168:175], v[214:221], v[34:49], v233, v232 op_sel_hi:[0,0,0]
	v_mfma_scale_f32_32x32x64_f8f6f4 v[2:17], v[168:175], v[222:229], v[2:17], v233, v232 op_sel_hi:[0,0,0]
	v_mfma_scale_f32_32x32x64_f8f6f4 v[50:65], v[176:183], v[198:205], v[50:65], v232, v232 op_sel_hi:[0,0,0]
	v_mfma_scale_f32_32x32x64_f8f6f4 v[18:33], v[176:183], v[206:213], v[18:33], v232, v232 op_sel_hi:[0,0,0]
	v_mfma_scale_f32_32x32x64_f8f6f4 v[50:65], v[184:191], v[214:221], v[50:65], v232, v232 op_sel_hi:[0,0,0]
	v_mfma_scale_f32_32x32x64_f8f6f4 v[18:33], v[184:191], v[222:229], v[18:33], v232, v232 op_sel_hi:[0,0,0]
	s_setprio 0
	s_barrier
	s_add_i32 s66, s66, 2
	s_add_u32 s64, s64, 0x10000
	s_addc_u32 s65, s65, 0
	s_add_u32 s40, s40, 0x100
	s_addc_u32 s41, s41, 0
	s_cmp_gt_u32 s66, 13
	s_cbranch_scc0 .LBB0_1896
	s_and_b64 vcc, exec, s[8:9]
	s_cbranch_vccz .LBB0_1899
	s_barrier

; #define PG8_STAGE(bufoff, gbase, voff) do { _Pragma("unroll") for (int _i = 0; _i < 2; ++_i) \
;         __builtin_amdgcn_global_load_lds((const unsigned*)((const char*)(gbase) + (voff)[_i]), (PG8_LAS unsigned*)(lds + (bufoff) + ldsw + _i * 8192), 16, 0, 0); } while (0)
; #define PG8_LDA(dst, b, h) do { _Pragma("unroll") for (int m = 0; m < 4; ++m) _Pragma("unroll") for (int k = 0; k < 2; ++k) dst[m][k] = *(const PG8_LAS bf16x8*)(lds + PG8_SA(b, h) + aoff + m * 2048 + k * 1024); } while (0)
; #define PG8_LDB(dst, b, h) do { _Pragma("unroll") for (int n = 0; n < 2; ++n) _Pragma("unroll") for (int k = 0; k < 2; ++k) dst[n][k] = *(const PG8_LAS bf16x8*)(lds + PG8_SB(b, h) + boff + n * 2048 + k * 1024); } while (0)
; #define PG8_WAIT_V(n) asm volatile("s_waitcnt vmcnt(" #n ")" ::: "memory")
; #define PG8_WAIT_L(n) asm volatile("s_waitcnt lgkmcnt(" #n ")" ::: "memory")
; #define PG8_BAR __builtin_amdgcn_s_barrier()
; #define PG8_SCHED __builtin_amdgcn_sched_barrier(0)
; #define PG8_WAIT_V(n) asm volatile("s_waitcnt vmcnt(" #n ")" ::: "memory")
; template <class Epi, class Sched, int SCW, int SCX, int SCW1 = SCW>
; __device__ __forceinline__ void gemm_phase_f8(PG8_LAS unsigned char* lds, const Gemm g, const Sched& S, const Epi& E, const int tid) {
;     ...
;         const char* nA = has_next ? (const char*)g.A + (size_t)nxt.pm * tstep + (size_t)nxt.k0 : cA; const char* nB = has_next ? (const char*)g.Bt + (size_t)nxt.pn * tstep + (size_t)nxt.k0 * 256 : cB;
;         for (int t = 0; t < nt; t += 2) {
;             const bool last = (t == nt - 2);
;             const char* a1 = cA + (size_t)(t + 1) * kstep;
;             const char* a2 = last ? nA : cA + (size_t)(t + 2) * kstep; const char* b2 = last ? nB : cB + (size_t)(t + 2) * kstepB;
;             const char* a3 = a2 + kstep; const char* b3 = b2 + kstepB;
;             if (last && has_next) S.a_ready(nxt);
;             PG8_LDB(B0, 0, 0); PG8_LDB(B1, 0, 1); PG8_SCHED; PG8_LDA(At, 0, 0); PG8_STAGE(PG8_SA(1, 1), a1 + hstep, voffA);
;             PG8_WAIT_V(8); PG8_WAIT_L(0); PG8_BAR; PG8_MMA(0, 0, At, B0); PG8_MMA(0, 1, At, B1); PG8_BAR; PG8_SCHED;
;             PG8_LDA(At, 0, 1); PG8_STAGE(PG8_SB(0, 0), b2, voffB); PG8_STAGE(PG8_SB(0, 1), b2 + hstepB, voffB); PG8_STAGE(PG8_SA(0, 0), a2, voffA);
;             PG8_WAIT_V(8); PG8_WAIT_L(0); PG8_BAR; PG8_MMA(1, 0, At, B0); PG8_MMA(1, 1, At, B1); PG8_BAR; PG8_SCHED;
.LBB0_2000:
	s_add_i32 s63, s6, 2
	s_add_u32 s7, s28, 0x4000
	s_addc_u32 s30, s29, 0
	s_add_i32 s66, 0, 0x10000
	s_cmp_eq_u32 s12, s6
	v_add_u32_e32 v153, s66, v131
	v_add_u32_e32 v158, s66, v144
	s_cselect_b32 s31, s21, s30
	s_cselect_b32 s30, s20, s7
	ds_read_b128 v[154:157], v153
	ds_read_b128 v[158:161], v158
	v_add_u32_e32 v153, s66, v145
	v_add_u32_e32 v166, s66, v146
	s_cselect_b32 s7, s23, s17
	s_cselect_b32 s6, s22, s13
	s_add_i32 s87, 0, 0x14000
	ds_read_b128 v[162:165], v153
	ds_read_b128 v[166:169], v166
	v_add_u32_e32 v153, s87, v131
	v_add_u32_e32 v174, s87, v144
	ds_read_b128 v[170:173], v153
	ds_read_b128 v[174:177], v174
	v_add_u32_e32 v153, s87, v145
	v_add_u32_e32 v182, s87, v146
	ds_read_b128 v[178:181], v153
	ds_read_b128 v[182:185], v182
	v_lshl_add_u64 v[194:195], s[28:29], 0, v[140:141]
	s_add_i32 m0, s51, 0xc000
	ds_read_b128 v[186:189], v149
	ds_read_b128 v[198:201], v149 offset:4096
	ds_read_b128 v[190:193], v150
	ds_read_b128 v[202:205], v150 offset:4096
	ds_read_b128 v[206:209], v151
	ds_read_b128 v[214:217], v151 offset:4096
	ds_read_b128 v[210:213], v152
	ds_read_b128 v[218:221], v152 offset:4096
	global_load_lds_dwordx4 v[194:195], off
	v_lshl_add_u64 v[194:195], s[28:29], 0, v[142:143]
	s_add_i32 m0, s51, 0xe000
	s_nop 0
	global_load_lds_dwordx4 v[194:195], off
	s_waitcnt vmcnt(8)
	s_waitcnt lgkmcnt(0)
	s_barrier
	s_setprio 1
	s_waitcnt lgkmcnt(0)
	v_mfma_scale_f32_32x32x64_f8f6f4 v[114:129], v[154:161], v[186:193], v[114:129], v233, v234 op_sel_hi:[0,0,0]
	v_mfma_scale_f32_32x32x64_f8f6f4 v[82:97], v[154:161], v[198:205], v[82:97], v233, v234 op_sel_hi:[0,0,0]
	v_mfma_scale_f32_32x32x64_f8f6f4 v[114:129], v[162:169], v[206:213], v[114:129], v233, v234 op_sel_hi:[0,0,0]
	v_mfma_scale_f32_32x32x64_f8f6f4 v[82:97], v[162:169], v[214:221], v[82:97], v233, v234 op_sel_hi:[0,0,0]
	v_mfma_scale_f32_32x32x64_f8f6f4 v[98:113], v[170:177], v[186:193], v[98:113], v233, v234 op_sel_hi:[0,0,0]
	v_mfma_scale_f32_32x32x64_f8f6f4 v[66:81], v[170:177], v[198:205], v[66:81], v233, v234 op_sel_hi:[0,0,0]
	v_mfma_scale_f32_32x32x64_f8f6f4 v[98:113], v[178:185], v[206:213], v[98:113], v233, v234 op_sel_hi:[0,0,0]
	v_mfma_scale_f32_32x32x64_f8f6f4 v[66:81], v[178:185], v[214:221], v[66:81], v233, v234 op_sel_hi:[0,0,0]
	s_setprio 0
	s_barrier
	s_add_i32 s66, s66, s50
	v_lshl_add_u64 v[194:195], s[6:7], 0, v[134:135]
	s_mov_b32 m0, s66
	ds_read_b128 v[186:189], v149 offset:16384
	ds_read_b128 v[198:201], v149 offset:20480
	ds_read_b128 v[190:193], v150 offset:16384
	ds_read_b128 v[202:205], v150 offset:20480
	ds_read_b128 v[206:209], v151 offset:16384
	ds_read_b128 v[214:217], v151 offset:20480
	ds_read_b128 v[210:213], v152 offset:16384
	ds_read_b128 v[218:221], v152 offset:20480
	global_load_lds_dwordx4 v[194:195], off
	s_add_i32 m0, s66, 0x2000
	s_add_u32 s88, s6, 0x4000
	v_lshl_add_u64 v[194:195], s[6:7], 0, v[138:139]
	s_addc_u32 s89, s7, 0
	s_add_i32 s66, s87, s50
	global_load_lds_dwordx4 v[194:195], off
	v_lshl_add_u64 v[194:195], s[88:89], 0, v[134:135]
	s_mov_b32 m0, s66
	v_lshl_add_u64 v[222:223], s[30:31], 0, v[136:137]
	global_load_lds_dwordx4 v[194:195], off
	v_lshl_add_u64 v[194:195], s[88:89], 0, v[138:139]
	s_add_i32 m0, s66, 0x2000
	s_nop 0
	global_load_lds_dwordx4 v[194:195], off
	v_lshl_add_u64 v[194:195], s[30:31], 0, v[132:133]
	s_mov_b32 m0, s51
	s_nop 0
	global_load_lds_dwordx4 v[194:195], off
	s_mov_b32 m0, s52
	s_nop 0
	global_load_lds_dwordx4 v[222:223], off
	s_waitcnt vmcnt(8)
	s_waitcnt lgkmcnt(0)
	s_barrier
	s_setprio 1
	s_waitcnt lgkmcnt(0)
	v_mfma_scale_f32_32x32x64_f8f6f4 v[50:65], v[154:161], v[186:193], v[50:65], v233, v234 op_sel_hi:[0,0,0]
	v_mfma_scale_f32_32x32x64_f8f6f4 v[18:33], v[154:161], v[198:205], v[18:33], v233, v234 op_sel_hi:[0,0,0]
	v_mfma_scale_f32_32x32x64_f8f6f4 v[50:65], v[162:169], v[206:213], v[50:65], v233, v234 op_sel_hi:[0,0,0]
	v_mfma_scale_f32_32x32x64_f8f6f4 v[18:33], v[162:169], v[214:221], v[18:33], v233, v234 op_sel_hi:[0,0,0]
	v_mfma_scale_f32_32x32x64_f8f6f4 v[34:49], v[170:177], v[186:193], v[34:49], v233, v234 op_sel_hi:[0,0,0]
	v_mfma_scale_f32_32x32x64_f8f6f4 v[2:17], v[170:177], v[198:205], v[2:17], v233, v234 op_sel_hi:[0,0,0]
	v_mfma_scale_f32_32x32x64_f8f6f4 v[34:49], v[178:185], v[206:213], v[34:49], v233, v234 op_sel_hi:[0,0,0]
	v_mfma_scale_f32_32x32x64_f8f6f4 v[2:17], v[178:185], v[214:221], v[2:17], v233, v234 op_sel_hi:[0,0,0]
	s_setprio 0
	s_barrier
; #define PG8_STAGE(bufoff, gbase, voff) do { _Pragma("unroll") for (int _i = 0; _i < 2; ++_i) \
;         __builtin_amdgcn_global_load_lds((const unsigned*)((const char*)(gbase) + (voff)[_i]), (PG8_LAS unsigned*)(lds + (bufoff) + ldsw + _i * 8192), 16, 0, 0); } while (0)
; #define PG8_LDA(dst, b, h) do { _Pragma("unroll") for (int m = 0; m < 4; ++m) _Pragma("unroll") for (int k = 0; k < 2; ++k) dst[m][k] = *(const PG8_LAS bf16x8*)(lds + PG8_SA(b, h) + aoff + m * 2048 + k * 1024); } while (0)
; #define PG8_LDB(dst, b, h) do { _Pragma("unroll") for (int n = 0; n < 2; ++n) _Pragma("unroll") for (int k = 0; k < 2; ++k) dst[n][k] = *(const PG8_LAS bf16x8*)(lds + PG8_SB(b, h) + boff + n * 2048 + k * 1024); } while (0)
; #define PG8_MMA(ai, bj, At, Bt) do { __builtin_amdgcn_s_setprio(1); _Pragma("unroll") for (int m = 0; m < 4; ++m) _Pragma("unroll") for (int n = 0; n < 2; ++n) _Pragma("unroll") for (int k = 0; k < 2; ++k) \
;         acc[ai][bj][m][n] = __builtin_amdgcn_mfma_f32_16x16x32_bf16(Bt[n][k], At[m][k], acc[ai][bj][m][n], 0, 0, 0); __builtin_amdgcn_s_setprio(0); } while (0)
; #define PG8_WAIT_V(n) asm volatile("s_waitcnt vmcnt(" #n ")" ::: "memory")
; #define PG8_WAIT_L(n) asm volatile("s_waitcnt lgkmcnt(" #n ")" ::: "memory")
; #define PG8_BAR __builtin_amdgcn_s_barrier()
; #define PG8_SCHED __builtin_amdgcn_sched_barrier(0)
; #define PG8_STAGE(bufoff, gbase, voff) do { _Pragma("unroll") for (int _i = 0; _i < 2; ++_i) \
;         __builtin_amdgcn_global_load_lds((const unsigned*)((const char*)(gbase) + (voff)[_i]), (PG8_LAS unsigned*)(lds + (bufoff) + ldsw + _i * 8192), 16, 0, 0); } while (0)
; template <class Epi, class Sched, int SCW, int SCX, int SCW1 = SCW>
; __device__ __forceinline__ void gemm_phase_f8(PG8_LAS unsigned char* lds, const Gemm g, const Sched& S, const Epi& E, const int tid) {
;     ...
;             PG8_LDB(B0, 1, 0); PG8_LDB(B1, 1, 1); PG8_SCHED; PG8_LDA(At, 1, 0); PG8_STAGE(PG8_SA(0, 1), a2 + hstep, voffA);
;             PG8_WAIT_V(8); PG8_WAIT_L(0); PG8_BAR; PG8_MMA(0, 0, At, B0); PG8_MMA(0, 1, At, B1); PG8_BAR; PG8_SCHED;
;             PG8_LDA(At, 1, 1); PG8_STAGE(PG8_SB(1, 0), b3, voffB); PG8_STAGE(PG8_SB(1, 1), b3 + hstepB, voffB); PG8_STAGE(PG8_SA(1, 0), a3, voffA);
;             PG8_WAIT_V(8); PG8_WAIT_L(0); PG8_BAR; PG8_MMA(1, 0, At, B0); PG8_MMA(1, 1, At, B1); PG8_BAR; PG8_SCHED;
;         }
	s_add_i32 s66, 0, 0x18000
	v_add_u32_e32 v153, s66, v131
	v_add_u32_e32 v158, s66, v144
	ds_read_b128 v[154:157], v153
	ds_read_b128 v[158:161], v158
	v_add_u32_e32 v153, s66, v145
	v_add_u32_e32 v166, s66, v146
	s_add_i32 s87, 0, 0x1c000
	ds_read_b128 v[162:165], v153
	ds_read_b128 v[166:169], v166
	v_add_u32_e32 v153, s87, v131
	v_add_u32_e32 v174, s87, v144
	ds_read_b128 v[170:173], v153
	ds_read_b128 v[174:177], v174
	v_add_u32_e32 v153, s87, v145
	v_add_u32_e32 v182, s87, v146
	ds_read_b128 v[178:181], v153
	ds_read_b128 v[182:185], v182
	s_add_u32 s30, s30, 0x4000
	s_addc_u32 s31, s31, 0
	s_mov_b32 m0, s53
	v_lshl_add_u64 v[224:225], s[30:31], 0, v[132:133]
	ds_read_b128 v[186:189], v149 offset:32768
	ds_read_b128 v[198:201], v149 offset:36864
	ds_read_b128 v[190:193], v150 offset:32768
	ds_read_b128 v[202:205], v150 offset:36864
	ds_read_b128 v[206:209], v151 offset:32768
	ds_read_b128 v[214:217], v151 offset:36864
	ds_read_b128 v[210:213], v152 offset:32768
	ds_read_b128 v[218:221], v152 offset:36864
	global_load_lds_dwordx4 v[224:225], off
	v_lshl_add_u64 v[224:225], s[30:31], 0, v[136:137]
	s_mov_b32 m0, s54
	s_nop 0
	global_load_lds_dwordx4 v[224:225], off
	s_waitcnt vmcnt(8)
	s_waitcnt lgkmcnt(0)
	s_barrier
	s_setprio 1
	s_waitcnt lgkmcnt(0)
	v_mfma_scale_f32_32x32x64_f8f6f4 v[114:129], v[154:161], v[186:193], v[114:129], v233, v234 op_sel_hi:[0,0,0]
	v_mfma_scale_f32_32x32x64_f8f6f4 v[82:97], v[154:161], v[198:205], v[82:97], v233, v234 op_sel_hi:[0,0,0]
	v_mfma_scale_f32_32x32x64_f8f6f4 v[114:129], v[162:169], v[206:213], v[114:129], v233, v234 op_sel_hi:[0,0,0]
	v_mfma_scale_f32_32x32x64_f8f6f4 v[82:97], v[162:169], v[214:221], v[82:97], v233, v234 op_sel_hi:[0,0,0]
	v_mfma_scale_f32_32x32x64_f8f6f4 v[98:113], v[170:177], v[186:193], v[98:113], v233, v234 op_sel_hi:[0,0,0]
	v_mfma_scale_f32_32x32x64_f8f6f4 v[66:81], v[170:177], v[198:205], v[66:81], v233, v234 op_sel_hi:[0,0,0]
	v_mfma_scale_f32_32x32x64_f8f6f4 v[98:113], v[178:185], v[206:213], v[98:113], v233, v234 op_sel_hi:[0,0,0]
	v_mfma_scale_f32_32x32x64_f8f6f4 v[66:81], v[178:185], v[214:221], v[66:81], v233, v234 op_sel_hi:[0,0,0]
	s_setprio 0
	s_barrier
	s_add_u32 s30, s6, 0x8000
	s_addc_u32 s31, s7, 0
	s_add_i32 s66, s66, s50
	v_lshl_add_u64 v[224:225], s[30:31], 0, v[134:135]
	s_mov_b32 m0, s66
	ds_read_b128 v[186:189], v149 offset:49152
	ds_read_b128 v[198:201], v149 offset:53248
	ds_read_b128 v[190:193], v150 offset:49152
	ds_read_b128 v[202:205], v150 offset:53248
	ds_read_b128 v[206:209], v151 offset:49152
	ds_read_b128 v[214:217], v151 offset:53248
	ds_read_b128 v[210:213], v152 offset:49152
	ds_read_b128 v[218:221], v152 offset:53248
	global_load_lds_dwordx4 v[224:225], off
	s_add_i32 m0, s66, 0x2000
	s_add_u32 s6, s6, 0xc000
	v_lshl_add_u64 v[224:225], s[30:31], 0, v[138:139]
	s_addc_u32 s7, s7, 0
	s_add_i32 s30, s87, s50
	global_load_lds_dwordx4 v[224:225], off
	v_lshl_add_u64 v[224:225], s[6:7], 0, v[134:135]
	s_mov_b32 m0, s30
	v_lshl_add_u64 v[194:195], v[194:195], 0, s[100:101]
	global_load_lds_dwordx4 v[224:225], off
	v_lshl_add_u64 v[224:225], s[6:7], 0, v[138:139]
	s_add_i32 m0, s30, 0x2000
	s_nop 0
	global_load_lds_dwordx4 v[224:225], off
	s_mov_b32 m0, s59
	s_nop 0
	global_load_lds_dwordx4 v[194:195], off
	v_lshl_add_u64 v[194:195], v[222:223], 0, s[100:101]
	s_mov_b32 m0, s60
	s_nop 0
	global_load_lds_dwordx4 v[194:195], off
	s_waitcnt vmcnt(8)
	s_waitcnt lgkmcnt(0)
	s_barrier
	s_setprio 1
	s_waitcnt lgkmcnt(0)
	v_mfma_scale_f32_32x32x64_f8f6f4 v[50:65], v[154:161], v[186:193], v[50:65], v233, v234 op_sel_hi:[0,0,0]
	v_mfma_scale_f32_32x32x64_f8f6f4 v[18:33], v[154:161], v[198:205], v[18:33], v233, v234 op_sel_hi:[0,0,0]
	v_mfma_scale_f32_32x32x64_f8f6f4 v[50:65], v[162:169], v[206:213], v[50:65], v233, v234 op_sel_hi:[0,0,0]
	v_mfma_scale_f32_32x32x64_f8f6f4 v[18:33], v[162:169], v[214:221], v[18:33], v233, v234 op_sel_hi:[0,0,0]
	v_mfma_scale_f32_32x32x64_f8f6f4 v[34:49], v[170:177], v[186:193], v[34:49], v233, v234 op_sel_hi:[0,0,0]
	v_mfma_scale_f32_32x32x64_f8f6f4 v[2:17], v[170:177], v[198:205], v[2:17], v233, v234 op_sel_hi:[0,0,0]
	v_mfma_scale_f32_32x32x64_f8f6f4 v[34:49], v[178:185], v[206:213], v[34:49], v233, v234 op_sel_hi:[0,0,0]
	v_mfma_scale_f32_32x32x64_f8f6f4 v[2:17], v[178:185], v[214:221], v[2:17], v233, v234 op_sel_hi:[0,0,0]
	s_setprio 0
	s_barrier
	s_add_u32 s13, s13, 0x10000
	s_addc_u32 s17, s17, 0
	s_add_u32 s28, s28, 0x10000
	s_addc_u32 s29, s29, 0
	s_cmp_ge_i32 s63, s24
	s_mov_b32 s6, s63
	s_cbranch_scc0 .LBB0_2000
	s_and_b64 vcc, exec, s[8:9]
	s_cbranch_vccz .LBB0_2003
	s_barrier

; #define PG8_STAGE(bufoff, gbase, voff) do { _Pragma("unroll") for (int _i = 0; _i < 2; ++_i) \
;         __builtin_amdgcn_global_load_lds((const unsigned*)((const char*)(gbase) + (voff)[_i]), (PG8_LAS unsigned*)(lds + (bufoff) + ldsw + _i * 8192), 16, 0, 0); } while (0)
; #define PG8_LDA(dst, b, h) do { _Pragma("unroll") for (int m = 0; m < 4; ++m) _Pragma("unroll") for (int k = 0; k < 2; ++k) dst[m][k] = *(const PG8_LAS bf16x8*)(lds + PG8_SA(b, h) + aoff + m * 2048 + k * 1024); } while (0)
; #define PG8_LDB(dst, b, h) do { _Pragma("unroll") for (int n = 0; n < 2; ++n) _Pragma("unroll") for (int k = 0; k < 2; ++k) dst[n][k] = *(const PG8_LAS bf16x8*)(lds + PG8_SB(b, h) + boff + n * 2048 + k * 1024); } while (0)
; #define PG8_WAIT_V(n) asm volatile("s_waitcnt vmcnt(" #n ")" ::: "memory")
; #define PG8_WAIT_L(n) asm volatile("s_waitcnt lgkmcnt(" #n ")" ::: "memory")
; #define PG8_BAR __builtin_amdgcn_s_barrier()
; #define PG8_SCHED __builtin_amdgcn_sched_barrier(0)
; #define PG8_BAR __builtin_amdgcn_s_barrier()
; template <class Epi, class Sched, bool ALIGN_EPI = false, bool SP2 = false>
; __device__ __forceinline__ void gemm_phase(PG8_LAS unsigned char* lds, const Gemm g, const Sched& S, const Epi& E, const int tid) {
;     ...
;         const char* nA = has_next ? (const char*)g.A + (size_t)nxt.pm * tstep + (size_t)nxt.k0 * 2 : cA; const char* nB = has_next ? (const char*)g.Bt + (size_t)nxt.pn * tstep + (size_t)nxt.k0 * 2 : cB;
;         for (int t = 0; t < nt; t += 2) {
;             const bool last = (t == nt - 2);
;             const char* a1 = cA + (size_t)(t + 1) * kstep;
;             const char* a2 = last ? nA : cA + (size_t)(t + 2) * kstep; const char* b2 = last ? nB : cB + (size_t)(t + 2) * kstep;
;             const char* a3 = a2 + kstep; const char* b3 = b2 + kstep;
;             if (last && has_next) S.a_ready(nxt);
;             if constexpr (SP2) {
;             PG8_LDB(B0, 0, 0); PG8_LDB(B1, 0, 1); PG8_SCHED; PG8_LDA(At, 0, 0); PG8_STAGE(PG8_SA(1, 1), a1 + hstep, voffA);
;             PG8_WAIT_V(8); PG8_WAIT_L(0); PG8_BAR; PG8_MMA(0, 0, At, B0); PG8_MMA(0, 1, At, B1); PG8_BAR; PG8_SCHED;
;             PG8_LDA(At, 0, 1); PG8_STAGE(PG8_SB(0, 0), b2, voffB); PG8_STAGE(PG8_SB(0, 1), b2 + hstep, voffB); PG8_STAGE(PG8_SA(0, 0), a2, voffA);
;             PG8_WAIT_V(8); PG8_WAIT_L(0); PG8_BAR; PG8_MMA(1, 0, At, B0); PG8_MMA(1, 1, At, B1); PG8_BAR; PG8_SCHED;
.LBB0_2282:
	s_add_u32 s6, s54, 0xfff80080
	s_addc_u32 s7, s55, -1
	s_add_i32 s26, 0, 0x10000
	s_cmp_eq_u32 s24, 28
	s_cselect_b32 s57, s5, s7
	s_cselect_b32 s56, s12, s6
	v_add_u32_e32 v131, s26, v156
	s_cselect_b32 s7, s13, s19
	s_cselect_b32 s6, s15, s18
	s_add_i32 s31, 0, 0x14000
	ds_read_b128 v[172:175], v131
	ds_read_b128 v[176:179], v131 offset:1024
	ds_read_b128 v[180:183], v131 offset:2048
	ds_read_b128 v[184:187], v131 offset:3072
	v_add_u32_e32 v131, s31, v156
	ds_read_b128 v[188:191], v131
	ds_read_b128 v[192:195], v131 offset:1024
	ds_read_b128 v[198:201], v131 offset:2048
	ds_read_b128 v[202:205], v131 offset:3072
	v_lshl_add_u64 v[132:133], s[54:55], 0, v[148:149]
	s_add_i32 m0, s65, 0xc000
	ds_read_b128 v[206:209], v170
	ds_read_b128 v[210:213], v170 offset:1024
	ds_read_b128 v[214:217], v170 offset:2048
	ds_read_b128 v[218:221], v170 offset:3072
	ds_read_b128 v[222:225], v170 offset:4096
	ds_read_b128 v[226:229], v170 offset:5120
	ds_read_b128 v[244:247], v170 offset:6144
	ds_read_b128 v[248:251], v170 offset:7168
	global_load_lds_dwordx4 v[132:133], off
	v_lshl_add_u64 v[132:133], s[54:55], 0, v[150:151]
	s_add_i32 m0, s65, 0xe000
	s_nop 0
	global_load_lds_dwordx4 v[132:133], off
	s_waitcnt vmcnt(8)
	s_waitcnt lgkmcnt(0)
	s_barrier
	s_setprio 1
	s_waitcnt lgkmcnt(0)
	v_mfma_f32_16x16x32_bf16 v[122:125], v[172:175], v[206:209], v[122:125]
	v_mfma_f32_16x16x32_bf16 v[114:117], v[180:183], v[206:209], v[114:117]
	v_mfma_f32_16x16x32_bf16 v[106:109], v[172:175], v[214:217], v[106:109]
	v_mfma_f32_16x16x32_bf16 v[98:101], v[180:183], v[214:217], v[98:101]
	v_mfma_f32_16x16x32_bf16 v[90:93], v[172:175], v[222:225], v[90:93]
	v_mfma_f32_16x16x32_bf16 v[82:85], v[180:183], v[222:225], v[82:85]
	v_mfma_f32_16x16x32_bf16 v[74:77], v[172:175], v[244:247], v[74:77]
	v_mfma_f32_16x16x32_bf16 v[66:69], v[180:183], v[244:247], v[66:69]
	v_mfma_f32_16x16x32_bf16 v[122:125], v[176:179], v[210:213], v[122:125]
	v_mfma_f32_16x16x32_bf16 v[114:117], v[184:187], v[210:213], v[114:117]
	v_mfma_f32_16x16x32_bf16 v[106:109], v[176:179], v[218:221], v[106:109]
	v_mfma_f32_16x16x32_bf16 v[98:101], v[184:187], v[218:221], v[98:101]
	v_mfma_f32_16x16x32_bf16 v[90:93], v[176:179], v[226:229], v[90:93]
	v_mfma_f32_16x16x32_bf16 v[82:85], v[184:187], v[226:229], v[82:85]
	v_mfma_f32_16x16x32_bf16 v[74:77], v[176:179], v[248:251], v[74:77]
	v_mfma_f32_16x16x32_bf16 v[66:69], v[184:187], v[248:251], v[66:69]
	v_mfma_f32_16x16x32_bf16 v[126:129], v[188:191], v[206:209], v[126:129]
	v_mfma_f32_16x16x32_bf16 v[118:121], v[198:201], v[206:209], v[118:121]
	v_mfma_f32_16x16x32_bf16 v[110:113], v[188:191], v[214:217], v[110:113]
	v_mfma_f32_16x16x32_bf16 v[102:105], v[198:201], v[214:217], v[102:105]
	v_mfma_f32_16x16x32_bf16 v[94:97], v[188:191], v[222:225], v[94:97]
	v_mfma_f32_16x16x32_bf16 v[86:89], v[198:201], v[222:225], v[86:89]
	v_mfma_f32_16x16x32_bf16 v[78:81], v[188:191], v[244:247], v[78:81]
	v_mfma_f32_16x16x32_bf16 v[70:73], v[198:201], v[244:247], v[70:73]
	v_mfma_f32_16x16x32_bf16 v[126:129], v[192:195], v[210:213], v[126:129]
	v_mfma_f32_16x16x32_bf16 v[118:121], v[202:205], v[210:213], v[118:121]
	v_mfma_f32_16x16x32_bf16 v[110:113], v[192:195], v[218:221], v[110:113]
	v_mfma_f32_16x16x32_bf16 v[102:105], v[202:205], v[218:221], v[102:105]
	v_mfma_f32_16x16x32_bf16 v[94:97], v[192:195], v[226:229], v[94:97]
	v_mfma_f32_16x16x32_bf16 v[86:89], v[202:205], v[226:229], v[86:89]
	v_mfma_f32_16x16x32_bf16 v[78:81], v[192:195], v[248:251], v[78:81]
	v_mfma_f32_16x16x32_bf16 v[70:73], v[202:205], v[248:251], v[70:73]
	s_setprio 0
	s_barrier
	s_add_i32 s26, s26, s64
	v_lshl_add_u64 v[132:133], s[6:7], 0, v[136:137]
	s_mov_b32 m0, s26
	ds_read_b128 v[206:209], v170 offset:16384
	ds_read_b128 v[210:213], v170 offset:17408
	ds_read_b128 v[214:217], v170 offset:18432
	ds_read_b128 v[218:221], v170 offset:19456
	ds_read_b128 v[222:225], v170 offset:20480
	ds_read_b128 v[226:229], v170 offset:21504
	ds_read_b128 v[244:247], v170 offset:22528
	ds_read_b128 v[248:251], v170 offset:23552
	global_load_lds_dwordx4 v[132:133], off
	s_add_i32 m0, s26, 0x2000
	s_add_u32 s36, s6, 0x80000
	v_lshl_add_u64 v[152:153], s[6:7], 0, v[140:141]
	s_addc_u32 s37, s7, 0
	s_add_i32 s26, s31, s64
	global_load_lds_dwordx4 v[152:153], off
	v_lshl_add_u64 v[230:231], s[36:37], 0, v[136:137]
	s_mov_b32 m0, s26
	v_lshl_add_u64 v[242:243], s[56:57], 0, v[138:139]
	global_load_lds_dwordx4 v[230:231], off
	v_lshl_add_u64 v[230:231], s[36:37], 0, v[140:141]
	s_add_i32 m0, s26, 0x2000
	s_nop 0
	global_load_lds_dwordx4 v[230:231], off
	v_lshl_add_u64 v[230:231], s[56:57], 0, v[134:135]
	s_mov_b32 m0, s65
	s_nop 0
	global_load_lds_dwordx4 v[230:231], off
	s_mov_b32 m0, s68
	s_nop 0
	global_load_lds_dwordx4 v[242:243], off
	s_waitcnt vmcnt(8)
	s_waitcnt lgkmcnt(0)
	s_barrier
; #define PG8_STAGE(bufoff, gbase, voff) do { _Pragma("unroll") for (int _i = 0; _i < 2; ++_i) \
;         __builtin_amdgcn_global_load_lds((const unsigned*)((const char*)(gbase) + (voff)[_i]), (PG8_LAS unsigned*)(lds + (bufoff) + ldsw + _i * 8192), 16, 0, 0); } while (0)
; #define PG8_LDA(dst, b, h) do { _Pragma("unroll") for (int m = 0; m < 4; ++m) _Pragma("unroll") for (int k = 0; k < 2; ++k) dst[m][k] = *(const PG8_LAS bf16x8*)(lds + PG8_SA(b, h) + aoff + m * 2048 + k * 1024); } while (0)
; #define PG8_LDB(dst, b, h) do { _Pragma("unroll") for (int n = 0; n < 2; ++n) _Pragma("unroll") for (int k = 0; k < 2; ++k) dst[n][k] = *(const PG8_LAS bf16x8*)(lds + PG8_SB(b, h) + boff + n * 2048 + k * 1024); } while (0)
; #define PG8_MMA(ai, bj, At, Bt) do { __builtin_amdgcn_s_setprio(1); _Pragma("unroll") for (int m = 0; m < 4; ++m) _Pragma("unroll") for (int n = 0; n < 2; ++n) _Pragma("unroll") for (int k = 0; k < 2; ++k) \
;         acc[ai][bj][m][n] = __builtin_amdgcn_mfma_f32_16x16x32_bf16(Bt[n][k], At[m][k], acc[ai][bj][m][n], 0, 0, 0); __builtin_amdgcn_s_setprio(0); } while (0)
; #define PG8_WAIT_V(n) asm volatile("s_waitcnt vmcnt(" #n ")" ::: "memory")
; #define PG8_WAIT_L(n) asm volatile("s_waitcnt lgkmcnt(" #n ")" ::: "memory")
; #define PG8_BAR __builtin_amdgcn_s_barrier()
; #define PG8_SCHED __builtin_amdgcn_sched_barrier(0)
; #define PG8_STAGE(bufoff, gbase, voff) do { _Pragma("unroll") for (int _i = 0; _i < 2; ++_i) \
;         __builtin_amdgcn_global_load_lds((const unsigned*)((const char*)(gbase) + (voff)[_i]), (PG8_LAS unsigned*)(lds + (bufoff) + ldsw + _i * 8192), 16, 0, 0); } while (0)
; #define PG8_BAR __builtin_amdgcn_s_barrier()
; template <class Epi, class Sched, bool ALIGN_EPI = false, bool SP2 = false>
; __device__ __forceinline__ void gemm_phase(PG8_LAS unsigned char* lds, const Gemm g, const Sched& S, const Epi& E, const int tid) {
;     ...
;             PG8_WAIT_V(8); PG8_WAIT_L(0); PG8_BAR; PG8_MMA(1, 0, At, B0); PG8_MMA(1, 1, At, B1); PG8_BAR; PG8_SCHED;
;             PG8_LDB(B0, 1, 0); PG8_LDB(B1, 1, 1); PG8_SCHED; PG8_LDA(At, 1, 0); PG8_STAGE(PG8_SA(0, 1), a2 + hstep, voffA);
;             PG8_WAIT_V(8); PG8_WAIT_L(0); PG8_BAR; PG8_MMA(0, 0, At, B0); PG8_MMA(0, 1, At, B1); PG8_BAR; PG8_SCHED;
;             PG8_LDA(At, 1, 1); PG8_STAGE(PG8_SB(1, 0), b3, voffB); PG8_STAGE(PG8_SB(1, 1), b3 + hstep, voffB); PG8_STAGE(PG8_SA(1, 0), a3, voffA);
	s_setprio 1
	s_waitcnt lgkmcnt(0)
	v_mfma_f32_16x16x32_bf16 v[58:61], v[172:175], v[206:209], v[58:61]
	v_mfma_f32_16x16x32_bf16 v[50:53], v[180:183], v[206:209], v[50:53]
	v_mfma_f32_16x16x32_bf16 v[42:45], v[172:175], v[214:217], v[42:45]
	v_mfma_f32_16x16x32_bf16 v[34:37], v[180:183], v[214:217], v[34:37]
	v_mfma_f32_16x16x32_bf16 v[26:29], v[172:175], v[222:225], v[26:29]
	v_mfma_f32_16x16x32_bf16 v[18:21], v[180:183], v[222:225], v[18:21]
	v_mfma_f32_16x16x32_bf16 v[10:13], v[172:175], v[244:247], v[10:13]
	v_mfma_f32_16x16x32_bf16 v[2:5], v[180:183], v[244:247], v[2:5]
	v_mfma_f32_16x16x32_bf16 v[58:61], v[176:179], v[210:213], v[58:61]
	v_mfma_f32_16x16x32_bf16 v[50:53], v[184:187], v[210:213], v[50:53]
	v_mfma_f32_16x16x32_bf16 v[42:45], v[176:179], v[218:221], v[42:45]
	v_mfma_f32_16x16x32_bf16 v[34:37], v[184:187], v[218:221], v[34:37]
	v_mfma_f32_16x16x32_bf16 v[26:29], v[176:179], v[226:229], v[26:29]
	v_mfma_f32_16x16x32_bf16 v[18:21], v[184:187], v[226:229], v[18:21]
	v_mfma_f32_16x16x32_bf16 v[10:13], v[176:179], v[248:251], v[10:13]
	v_mfma_f32_16x16x32_bf16 v[2:5], v[184:187], v[248:251], v[2:5]
	v_mfma_f32_16x16x32_bf16 v[62:65], v[188:191], v[206:209], v[62:65]
	v_mfma_f32_16x16x32_bf16 v[54:57], v[198:201], v[206:209], v[54:57]
	v_mfma_f32_16x16x32_bf16 v[46:49], v[188:191], v[214:217], v[46:49]
	v_mfma_f32_16x16x32_bf16 v[38:41], v[198:201], v[214:217], v[38:41]
	v_mfma_f32_16x16x32_bf16 v[30:33], v[188:191], v[222:225], v[30:33]
	v_mfma_f32_16x16x32_bf16 v[22:25], v[198:201], v[222:225], v[22:25]
	v_mfma_f32_16x16x32_bf16 v[14:17], v[188:191], v[244:247], v[14:17]
	v_mfma_f32_16x16x32_bf16 v[6:9], v[198:201], v[244:247], v[6:9]
	v_mfma_f32_16x16x32_bf16 v[62:65], v[192:195], v[210:213], v[62:65]
	v_mfma_f32_16x16x32_bf16 v[54:57], v[202:205], v[210:213], v[54:57]
	v_mfma_f32_16x16x32_bf16 v[46:49], v[192:195], v[218:221], v[46:49]
	v_mfma_f32_16x16x32_bf16 v[38:41], v[202:205], v[218:221], v[38:41]
	v_mfma_f32_16x16x32_bf16 v[30:33], v[192:195], v[226:229], v[30:33]
	v_mfma_f32_16x16x32_bf16 v[22:25], v[202:205], v[226:229], v[22:25]
	v_mfma_f32_16x16x32_bf16 v[14:17], v[192:195], v[248:251], v[14:17]
	v_mfma_f32_16x16x32_bf16 v[6:9], v[202:205], v[248:251], v[6:9]
	s_setprio 0
	s_barrier
	s_add_i32 s26, 0, 0x18000
	v_add_u32_e32 v131, s26, v156
	s_add_i32 s31, 0, 0x1c000
	ds_read_b128 v[172:175], v131
	ds_read_b128 v[176:179], v131 offset:1024
	ds_read_b128 v[180:183], v131 offset:2048
	ds_read_b128 v[184:187], v131 offset:3072
	v_add_u32_e32 v131, s31, v156
	ds_read_b128 v[188:191], v131
	ds_read_b128 v[192:195], v131 offset:1024
	ds_read_b128 v[198:201], v131 offset:2048
	ds_read_b128 v[202:205], v131 offset:3072
	s_add_u32 s36, s56, 0x80000
	s_addc_u32 s37, s57, 0
	s_mov_b32 m0, s69
	v_lshl_add_u64 v[158:159], s[36:37], 0, v[134:135]
	ds_read_b128 v[206:209], v170 offset:32768
	ds_read_b128 v[210:213], v170 offset:33792
	ds_read_b128 v[214:217], v170 offset:34816
	ds_read_b128 v[218:221], v170 offset:35840
	ds_read_b128 v[222:225], v170 offset:36864
	ds_read_b128 v[226:229], v170 offset:37888
	ds_read_b128 v[244:247], v170 offset:38912
	ds_read_b128 v[248:251], v170 offset:39936
	global_load_lds_dwordx4 v[158:159], off
	v_lshl_add_u64 v[158:159], s[36:37], 0, v[138:139]
	s_mov_b32 m0, s70
	s_nop 0
	global_load_lds_dwordx4 v[158:159], off
	s_waitcnt vmcnt(8)
	s_waitcnt lgkmcnt(0)
	s_barrier
	s_setprio 1
	s_waitcnt lgkmcnt(0)
	v_mfma_f32_16x16x32_bf16 v[122:125], v[172:175], v[206:209], v[122:125]
	v_mfma_f32_16x16x32_bf16 v[114:117], v[180:183], v[206:209], v[114:117]
	v_mfma_f32_16x16x32_bf16 v[106:109], v[172:175], v[214:217], v[106:109]
	v_mfma_f32_16x16x32_bf16 v[98:101], v[180:183], v[214:217], v[98:101]
	v_mfma_f32_16x16x32_bf16 v[90:93], v[172:175], v[222:225], v[90:93]
	v_mfma_f32_16x16x32_bf16 v[82:85], v[180:183], v[222:225], v[82:85]
	v_mfma_f32_16x16x32_bf16 v[74:77], v[172:175], v[244:247], v[74:77]
	v_mfma_f32_16x16x32_bf16 v[66:69], v[180:183], v[244:247], v[66:69]
	v_mfma_f32_16x16x32_bf16 v[122:125], v[176:179], v[210:213], v[122:125]
	v_mfma_f32_16x16x32_bf16 v[114:117], v[184:187], v[210:213], v[114:117]
	v_mfma_f32_16x16x32_bf16 v[106:109], v[176:179], v[218:221], v[106:109]
	v_mfma_f32_16x16x32_bf16 v[98:101], v[184:187], v[218:221], v[98:101]
	v_mfma_f32_16x16x32_bf16 v[90:93], v[176:179], v[226:229], v[90:93]
	v_mfma_f32_16x16x32_bf16 v[82:85], v[184:187], v[226:229], v[82:85]
	v_mfma_f32_16x16x32_bf16 v[74:77], v[176:179], v[248:251], v[74:77]
	v_mfma_f32_16x16x32_bf16 v[66:69], v[184:187], v[248:251], v[66:69]
	v_mfma_f32_16x16x32_bf16 v[126:129], v[188:191], v[206:209], v[126:129]
	v_mfma_f32_16x16x32_bf16 v[118:121], v[198:201], v[206:209], v[118:121]
	v_mfma_f32_16x16x32_bf16 v[110:113], v[188:191], v[214:217], v[110:113]
	v_mfma_f32_16x16x32_bf16 v[102:105], v[198:201], v[214:217], v[102:105]
	v_mfma_f32_16x16x32_bf16 v[94:97], v[188:191], v[222:225], v[94:97]
	v_mfma_f32_16x16x32_bf16 v[86:89], v[198:201], v[222:225], v[86:89]
	v_mfma_f32_16x16x32_bf16 v[78:81], v[188:191], v[244:247], v[78:81]
	v_mfma_f32_16x16x32_bf16 v[70:73], v[198:201], v[244:247], v[70:73]
	v_mfma_f32_16x16x32_bf16 v[126:129], v[192:195], v[210:213], v[126:129]
	v_mfma_f32_16x16x32_bf16 v[118:121], v[202:205], v[210:213], v[118:121]
	v_mfma_f32_16x16x32_bf16 v[110:113], v[192:195], v[218:221], v[110:113]
	v_mfma_f32_16x16x32_bf16 v[102:105], v[202:205], v[218:221], v[102:105]
	v_mfma_f32_16x16x32_bf16 v[94:97], v[192:195], v[226:229], v[94:97]
	v_mfma_f32_16x16x32_bf16 v[86:89], v[202:205], v[226:229], v[86:89]
	v_mfma_f32_16x16x32_bf16 v[78:81], v[192:195], v[248:251], v[78:81]
	v_mfma_f32_16x16x32_bf16 v[70:73], v[202:205], v[248:251], v[70:73]
	s_setprio 0
	s_barrier
; #define PG8_STAGE(bufoff, gbase, voff) do { _Pragma("unroll") for (int _i = 0; _i < 2; ++_i) \
;         __builtin_amdgcn_global_load_lds((const unsigned*)((const char*)(gbase) + (voff)[_i]), (PG8_LAS unsigned*)(lds + (bufoff) + ldsw + _i * 8192), 16, 0, 0); } while (0)
; #define PG8_LDA(dst, b, h) do { _Pragma("unroll") for (int m = 0; m < 4; ++m) _Pragma("unroll") for (int k = 0; k < 2; ++k) dst[m][k] = *(const PG8_LAS bf16x8*)(lds + PG8_SA(b, h) + aoff + m * 2048 + k * 1024); } while (0)
; #define PG8_MMA(ai, bj, At, Bt) do { __builtin_amdgcn_s_setprio(1); _Pragma("unroll") for (int m = 0; m < 4; ++m) _Pragma("unroll") for (int n = 0; n < 2; ++n) _Pragma("unroll") for (int k = 0; k < 2; ++k) \
;         acc[ai][bj][m][n] = __builtin_amdgcn_mfma_f32_16x16x32_bf16(Bt[n][k], At[m][k], acc[ai][bj][m][n], 0, 0, 0); __builtin_amdgcn_s_setprio(0); } while (0)
; #define PG8_WAIT_V(n) asm volatile("s_waitcnt vmcnt(" #n ")" ::: "memory")
; #define PG8_WAIT_L(n) asm volatile("s_waitcnt lgkmcnt(" #n ")" ::: "memory")
; #define PG8_BAR __builtin_amdgcn_s_barrier()
; #define PG8_SCHED __builtin_amdgcn_sched_barrier(0)
; #define PG8_STAGE(bufoff, gbase, voff) do { _Pragma("unroll") for (int _i = 0; _i < 2; ++_i) \
;         __builtin_amdgcn_global_load_lds((const unsigned*)((const char*)(gbase) + (voff)[_i]), (PG8_LAS unsigned*)(lds + (bufoff) + ldsw + _i * 8192), 16, 0, 0); } while (0)
; #define PG8_LDA(dst, b, h) do { _Pragma("unroll") for (int mb = 0; mb < 2; ++mb) _Pragma("unroll") for (int s = 0; s < 2; ++s) \
;         dst[mb][s] = cat8(*(const PG8_LAS bf16x8*)(lds + PG8_SA(b, h) + aoffk[s][0] + mb * 4096), *(const PG8_LAS bf16x8*)(lds + PG8_SA(b, h) + aoffk[s][1] + mb * 4096)); } while (0)
; template <class Epi, class Sched, bool ALIGN_EPI = false, bool SP2 = false>
; __device__ __forceinline__ void gemm_phase(PG8_LAS unsigned char* lds, const Gemm g, const Sched& S, const Epi& E, const int tid) {
;     ...
;         for (int t = 0; t < nt; t += 2) {
;     ...
;             PG8_WAIT_V(8); PG8_WAIT_L(0); PG8_BAR; PG8_MMA(0, 0, At, B0); PG8_MMA(0, 1, At, B1); PG8_BAR; PG8_SCHED;
;             PG8_LDA(At, 1, 1); PG8_STAGE(PG8_SB(1, 0), b3, voffB); PG8_STAGE(PG8_SB(1, 1), b3 + hstep, voffB); PG8_STAGE(PG8_SA(1, 0), a3, voffA);
;             PG8_WAIT_V(8); PG8_WAIT_L(0); PG8_BAR; PG8_MMA(1, 0, At, B0); PG8_MMA(1, 1, At, B1); PG8_BAR; PG8_SCHED;
	s_add_i32 s26, s26, s64
	v_lshl_add_u64 v[132:133], v[132:133], 0, s[34:35]
	s_mov_b32 m0, s26
	ds_read_b128 v[206:209], v170 offset:49152
	ds_read_b128 v[210:213], v170 offset:50176
	ds_read_b128 v[214:217], v170 offset:51200
	ds_read_b128 v[218:221], v170 offset:52224
	ds_read_b128 v[222:225], v170 offset:53248
	ds_read_b128 v[226:229], v170 offset:54272
	ds_read_b128 v[244:247], v170 offset:55296
	ds_read_b128 v[248:251], v170 offset:56320
	global_load_lds_dwordx4 v[132:133], off
	s_add_i32 m0, s26, 0x2000
	s_add_u32 s6, s6, 0x80080
	v_lshl_add_u64 v[132:133], v[152:153], 0, s[34:35]
	s_addc_u32 s7, s7, 0
	s_add_i32 s26, s31, s64
	global_load_lds_dwordx4 v[132:133], off
	v_lshl_add_u64 v[132:133], s[6:7], 0, v[136:137]
	s_mov_b32 m0, s26
	s_nop 0
	global_load_lds_dwordx4 v[132:133], off
	v_lshl_add_u64 v[132:133], s[6:7], 0, v[140:141]
	s_add_i32 m0, s26, 0x2000
	s_nop 0
	global_load_lds_dwordx4 v[132:133], off
	v_lshl_add_u64 v[132:133], v[230:231], 0, s[34:35]
	s_mov_b32 m0, s72
	s_nop 0
	global_load_lds_dwordx4 v[132:133], off
	v_lshl_add_u64 v[132:133], v[242:243], 0, s[34:35]
	s_mov_b32 m0, s73
	s_nop 0
	global_load_lds_dwordx4 v[132:133], off
	s_waitcnt vmcnt(8)
	s_waitcnt lgkmcnt(0)
	s_barrier
	s_setprio 1
	s_waitcnt lgkmcnt(0)
	v_mfma_f32_16x16x32_bf16 v[58:61], v[172:175], v[206:209], v[58:61]
	v_mfma_f32_16x16x32_bf16 v[50:53], v[180:183], v[206:209], v[50:53]
	v_mfma_f32_16x16x32_bf16 v[42:45], v[172:175], v[214:217], v[42:45]
	v_mfma_f32_16x16x32_bf16 v[34:37], v[180:183], v[214:217], v[34:37]
	v_mfma_f32_16x16x32_bf16 v[26:29], v[172:175], v[222:225], v[26:29]
	v_mfma_f32_16x16x32_bf16 v[18:21], v[180:183], v[222:225], v[18:21]
	v_mfma_f32_16x16x32_bf16 v[10:13], v[172:175], v[244:247], v[10:13]
	v_mfma_f32_16x16x32_bf16 v[2:5], v[180:183], v[244:247], v[2:5]
	v_mfma_f32_16x16x32_bf16 v[58:61], v[176:179], v[210:213], v[58:61]
	v_mfma_f32_16x16x32_bf16 v[50:53], v[184:187], v[210:213], v[50:53]
	v_mfma_f32_16x16x32_bf16 v[42:45], v[176:179], v[218:221], v[42:45]
	v_mfma_f32_16x16x32_bf16 v[34:37], v[184:187], v[218:221], v[34:37]
	v_mfma_f32_16x16x32_bf16 v[26:29], v[176:179], v[226:229], v[26:29]
	v_mfma_f32_16x16x32_bf16 v[18:21], v[184:187], v[226:229], v[18:21]
	v_mfma_f32_16x16x32_bf16 v[10:13], v[176:179], v[248:251], v[10:13]
	v_mfma_f32_16x16x32_bf16 v[2:5], v[184:187], v[248:251], v[2:5]
	v_mfma_f32_16x16x32_bf16 v[62:65], v[188:191], v[206:209], v[62:65]
	v_mfma_f32_16x16x32_bf16 v[54:57], v[198:201], v[206:209], v[54:57]
	v_mfma_f32_16x16x32_bf16 v[46:49], v[188:191], v[214:217], v[46:49]
	v_mfma_f32_16x16x32_bf16 v[38:41], v[198:201], v[214:217], v[38:41]
	v_mfma_f32_16x16x32_bf16 v[30:33], v[188:191], v[222:225], v[30:33]
	v_mfma_f32_16x16x32_bf16 v[22:25], v[198:201], v[222:225], v[22:25]
	v_mfma_f32_16x16x32_bf16 v[14:17], v[188:191], v[244:247], v[14:17]
	v_mfma_f32_16x16x32_bf16 v[6:9], v[198:201], v[244:247], v[6:9]
	v_mfma_f32_16x16x32_bf16 v[62:65], v[192:195], v[210:213], v[62:65]
	v_mfma_f32_16x16x32_bf16 v[54:57], v[202:205], v[210:213], v[54:57]
	v_mfma_f32_16x16x32_bf16 v[46:49], v[192:195], v[218:221], v[46:49]
	v_mfma_f32_16x16x32_bf16 v[38:41], v[202:205], v[218:221], v[38:41]
	v_mfma_f32_16x16x32_bf16 v[30:33], v[192:195], v[226:229], v[30:33]
	v_mfma_f32_16x16x32_bf16 v[22:25], v[202:205], v[226:229], v[22:25]
	v_mfma_f32_16x16x32_bf16 v[14:17], v[192:195], v[248:251], v[14:17]
	v_mfma_f32_16x16x32_bf16 v[6:9], v[202:205], v[248:251], v[6:9]
	s_setprio 0
	s_barrier
	s_add_i32 s24, s24, 2
	s_add_u32 s54, s54, 0x100
	s_addc_u32 s55, s55, 0
	s_add_u32 s18, s18, 0x100
	s_addc_u32 s19, s19, 0
	s_cmp_gt_u32 s24, 29
	s_cbranch_scc0 .LBB0_2282
	s_and_b64 vcc, exec, s[10:11]
	s_cbranch_vccz .LBB0_2285
	s_barrier

; #define PG8_STAGE(bufoff, gbase, voff) do { _Pragma("unroll") for (int _i = 0; _i < 2; ++_i) \
;         __builtin_amdgcn_global_load_lds((const unsigned*)((const char*)(gbase) + (voff)[_i]), (PG8_LAS unsigned*)(lds + (bufoff) + ldsw + _i * 8192), 16, 0, 0); } while (0)
; #define PG8_LDA(dst, b, h) do { _Pragma("unroll") for (int m = 0; m < 4; ++m) _Pragma("unroll") for (int k = 0; k < 2; ++k) dst[m][k] = *(const PG8_LAS bf16x8*)(lds + PG8_SA(b, h) + aoff + m * 2048 + k * 1024); } while (0)
; #define PG8_LDB(dst, b, h) do { _Pragma("unroll") for (int n = 0; n < 2; ++n) _Pragma("unroll") for (int k = 0; k < 2; ++k) dst[n][k] = *(const PG8_LAS bf16x8*)(lds + PG8_SB(b, h) + boff + n * 2048 + k * 1024); } while (0)
; #define PG8_WAIT_V(n) asm volatile("s_waitcnt vmcnt(" #n ")" ::: "memory")
; #define PG8_WAIT_L(n) asm volatile("s_waitcnt lgkmcnt(" #n ")" ::: "memory")
; #define PG8_BAR __builtin_amdgcn_s_barrier()
; #define PG8_SCHED __builtin_amdgcn_sched_barrier(0)
; #define PG8_BAR __builtin_amdgcn_s_barrier()
; template <class Epi, class Sched, bool ALIGN_EPI = false, bool SP2 = false>
; __device__ __forceinline__ void gemm_phase(PG8_LAS unsigned char* lds, const Gemm g, const Sched& S, const Epi& E, const int tid) {
;     ...
;         const char* nA = has_next ? (const char*)g.A + (size_t)nxt.pm * tstep + (size_t)nxt.k0 * 2 : cA; const char* nB = has_next ? (const char*)g.Bt + (size_t)nxt.pn * tstep + (size_t)nxt.k0 * 2 : cB;
;         for (int t = 0; t < nt; t += 2) {
;             const bool last = (t == nt - 2);
;             const char* a1 = cA + (size_t)(t + 1) * kstep;
;             const char* a2 = last ? nA : cA + (size_t)(t + 2) * kstep; const char* b2 = last ? nB : cB + (size_t)(t + 2) * kstep;
;             const char* a3 = a2 + kstep; const char* b3 = b2 + kstep;
;             if (last && has_next) S.a_ready(nxt);
;             if constexpr (SP2) {
;             PG8_LDB(B0, 0, 0); PG8_LDB(B1, 0, 1); PG8_SCHED; PG8_LDA(At, 0, 0); PG8_STAGE(PG8_SA(1, 1), a1 + hstep, voffA);
;             PG8_WAIT_V(8); PG8_WAIT_L(0); PG8_BAR; PG8_MMA(0, 0, At, B0); PG8_MMA(0, 1, At, B1); PG8_BAR; PG8_SCHED;
;             PG8_LDA(At, 0, 1); PG8_STAGE(PG8_SB(0, 0), b2, voffB); PG8_STAGE(PG8_SB(0, 1), b2 + hstep, voffB); PG8_STAGE(PG8_SA(0, 0), a2, voffA);
;             PG8_WAIT_V(8); PG8_WAIT_L(0); PG8_BAR; PG8_MMA(1, 0, At, B0); PG8_MMA(1, 1, At, B1); PG8_BAR; PG8_SCHED;
.LBB0_2525:
	s_add_i32 s19, s18, 2
	s_add_u32 s6, s22, 0x100
	s_addc_u32 s7, s23, 0
	s_add_i32 s26, 0, 0x10000
	s_cmp_eq_u32 s12, s18
	s_cselect_b32 s31, s17, s7
	s_cselect_b32 s30, s16, s6
	s_cselect_b32 s29, s21, s15
	s_cselect_b32 s28, s20, s13
	s_add_i32 s18, 0, 0x14000
	v_add_u32_e32 v144, s26, v162
	v_add_u32_e32 v160, s18, v162
	ds_read_b128 v[132:135], v144
	ds_read_b128 v[136:139], v144 offset:1024
	ds_read_b128 v[140:143], v144 offset:2048
	ds_read_b128 v[144:147], v144 offset:3072
	ds_read_b128 v[172:175], v160
	ds_read_b128 v[176:179], v160 offset:1024
	ds_read_b128 v[180:183], v160 offset:2048
	ds_read_b128 v[184:187], v160 offset:3072
	v_lshl_add_u64 v[160:161], s[22:23], 0, v[156:157]
	s_add_i32 m0, s44, 0xc000
	ds_read_b128 v[188:191], v171
	ds_read_b128 v[192:195], v171 offset:1024
	ds_read_b128 v[198:201], v171 offset:2048
	ds_read_b128 v[202:205], v171 offset:3072
	ds_read_b128 v[206:209], v171 offset:4096
	ds_read_b128 v[210:213], v171 offset:5120
	ds_read_b128 v[214:217], v171 offset:6144
	ds_read_b128 v[218:221], v171 offset:7168
	global_load_lds_dwordx4 v[160:161], off
	v_lshl_add_u64 v[160:161], s[22:23], 0, v[158:159]
	s_add_i32 m0, s44, 0xe000
	s_nop 0
	global_load_lds_dwordx4 v[160:161], off
	s_waitcnt vmcnt(8)
	s_waitcnt lgkmcnt(0)
	s_barrier
	s_setprio 1
	s_waitcnt lgkmcnt(0)
	v_mfma_f32_16x16x32_bf16 v[126:129], v[132:135], v[188:191], v[126:129]
	v_mfma_f32_16x16x32_bf16 v[122:125], v[140:143], v[188:191], v[122:125]
	v_mfma_f32_16x16x32_bf16 v[114:117], v[132:135], v[198:201], v[114:117]
	v_mfma_f32_16x16x32_bf16 v[106:109], v[140:143], v[198:201], v[106:109]
	v_mfma_f32_16x16x32_bf16 v[98:101], v[132:135], v[206:209], v[98:101]
	v_mfma_f32_16x16x32_bf16 v[90:93], v[140:143], v[206:209], v[90:93]
	v_mfma_f32_16x16x32_bf16 v[82:85], v[132:135], v[214:217], v[82:85]
	v_mfma_f32_16x16x32_bf16 v[74:77], v[140:143], v[214:217], v[74:77]
	v_mfma_f32_16x16x32_bf16 v[126:129], v[136:139], v[192:195], v[126:129]
	v_mfma_f32_16x16x32_bf16 v[122:125], v[144:147], v[192:195], v[122:125]
	v_mfma_f32_16x16x32_bf16 v[114:117], v[136:139], v[202:205], v[114:117]
	v_mfma_f32_16x16x32_bf16 v[106:109], v[144:147], v[202:205], v[106:109]
	v_mfma_f32_16x16x32_bf16 v[98:101], v[136:139], v[210:213], v[98:101]
	v_mfma_f32_16x16x32_bf16 v[90:93], v[144:147], v[210:213], v[90:93]
	v_mfma_f32_16x16x32_bf16 v[82:85], v[136:139], v[218:221], v[82:85]
	v_mfma_f32_16x16x32_bf16 v[74:77], v[144:147], v[218:221], v[74:77]
	v_mfma_f32_16x16x32_bf16 v[118:121], v[172:175], v[188:191], v[118:121]
	v_mfma_f32_16x16x32_bf16 v[110:113], v[180:183], v[188:191], v[110:113]
	v_mfma_f32_16x16x32_bf16 v[102:105], v[172:175], v[198:201], v[102:105]
	v_mfma_f32_16x16x32_bf16 v[94:97], v[180:183], v[198:201], v[94:97]
	v_mfma_f32_16x16x32_bf16 v[86:89], v[172:175], v[206:209], v[86:89]
	v_mfma_f32_16x16x32_bf16 v[78:81], v[180:183], v[206:209], v[78:81]
	v_mfma_f32_16x16x32_bf16 v[70:73], v[172:175], v[214:217], v[70:73]
	v_mfma_f32_16x16x32_bf16 v[66:69], v[180:183], v[214:217], v[66:69]
	v_mfma_f32_16x16x32_bf16 v[118:121], v[176:179], v[192:195], v[118:121]
	v_mfma_f32_16x16x32_bf16 v[110:113], v[184:187], v[192:195], v[110:113]
	v_mfma_f32_16x16x32_bf16 v[102:105], v[176:179], v[202:205], v[102:105]
	v_mfma_f32_16x16x32_bf16 v[94:97], v[184:187], v[202:205], v[94:97]
	v_mfma_f32_16x16x32_bf16 v[86:89], v[176:179], v[210:213], v[86:89]
	v_mfma_f32_16x16x32_bf16 v[78:81], v[184:187], v[210:213], v[78:81]
	v_mfma_f32_16x16x32_bf16 v[70:73], v[176:179], v[218:221], v[70:73]
	v_mfma_f32_16x16x32_bf16 v[66:69], v[184:187], v[218:221], v[66:69]
	s_setprio 0
	s_barrier
	s_add_i32 s22, s26, s43
	v_lshl_add_u64 v[160:161], s[28:29], 0, v[150:151]
	s_mov_b32 m0, s22
	ds_read_b128 v[188:191], v171 offset:16384
	ds_read_b128 v[192:195], v171 offset:17408
	ds_read_b128 v[198:201], v171 offset:18432
	ds_read_b128 v[202:205], v171 offset:19456
	ds_read_b128 v[206:209], v171 offset:20480
	ds_read_b128 v[210:213], v171 offset:21504
	ds_read_b128 v[214:217], v171 offset:22528
	ds_read_b128 v[218:221], v171 offset:23552
	global_load_lds_dwordx4 v[160:161], off
	s_add_i32 m0, s22, 0x2000
	s_add_u32 s22, s28, 0x160000
	v_lshl_add_u64 v[222:223], s[28:29], 0, v[154:155]
	s_addc_u32 s23, s29, 0
	s_add_i32 s18, s18, s43
	global_load_lds_dwordx4 v[222:223], off
	v_lshl_add_u64 v[224:225], s[22:23], 0, v[150:151]
	s_mov_b32 m0, s18
	v_lshl_add_u64 v[226:227], s[30:31], 0, v[152:153]
	global_load_lds_dwordx4 v[224:225], off
	v_lshl_add_u64 v[224:225], s[22:23], 0, v[154:155]
	s_add_i32 m0, s18, 0x2000
	s_nop 0
	global_load_lds_dwordx4 v[224:225], off
	v_lshl_add_u64 v[224:225], s[30:31], 0, v[148:149]
	s_mov_b32 m0, s44
	s_nop 0
	global_load_lds_dwordx4 v[224:225], off
	s_mov_b32 m0, s45
	s_nop 0
	global_load_lds_dwordx4 v[226:227], off
	s_waitcnt vmcnt(8)
	s_waitcnt lgkmcnt(0)
	s_barrier
; #define PG8_STAGE(bufoff, gbase, voff) do { _Pragma("unroll") for (int _i = 0; _i < 2; ++_i) \
;         __builtin_amdgcn_global_load_lds((const unsigned*)((const char*)(gbase) + (voff)[_i]), (PG8_LAS unsigned*)(lds + (bufoff) + ldsw + _i * 8192), 16, 0, 0); } while (0)
; #define PG8_LDA(dst, b, h) do { _Pragma("unroll") for (int m = 0; m < 4; ++m) _Pragma("unroll") for (int k = 0; k < 2; ++k) dst[m][k] = *(const PG8_LAS bf16x8*)(lds + PG8_SA(b, h) + aoff + m * 2048 + k * 1024); } while (0)
; #define PG8_LDB(dst, b, h) do { _Pragma("unroll") for (int n = 0; n < 2; ++n) _Pragma("unroll") for (int k = 0; k < 2; ++k) dst[n][k] = *(const PG8_LAS bf16x8*)(lds + PG8_SB(b, h) + boff + n * 2048 + k * 1024); } while (0)
; #define PG8_MMA(ai, bj, At, Bt) do { __builtin_amdgcn_s_setprio(1); _Pragma("unroll") for (int m = 0; m < 4; ++m) _Pragma("unroll") for (int n = 0; n < 2; ++n) _Pragma("unroll") for (int k = 0; k < 2; ++k) \
;         acc[ai][bj][m][n] = __builtin_amdgcn_mfma_f32_16x16x32_bf16(Bt[n][k], At[m][k], acc[ai][bj][m][n], 0, 0, 0); __builtin_amdgcn_s_setprio(0); } while (0)
; #define PG8_WAIT_V(n) asm volatile("s_waitcnt vmcnt(" #n ")" ::: "memory")
; #define PG8_WAIT_L(n) asm volatile("s_waitcnt lgkmcnt(" #n ")" ::: "memory")
; #define PG8_BAR __builtin_amdgcn_s_barrier()
; #define PG8_SCHED __builtin_amdgcn_sched_barrier(0)
; #define PG8_STAGE(bufoff, gbase, voff) do { _Pragma("unroll") for (int _i = 0; _i < 2; ++_i) \
;         __builtin_amdgcn_global_load_lds((const unsigned*)((const char*)(gbase) + (voff)[_i]), (PG8_LAS unsigned*)(lds + (bufoff) + ldsw + _i * 8192), 16, 0, 0); } while (0)
; #define PG8_BAR __builtin_amdgcn_s_barrier()
; template <class Epi, class Sched, bool ALIGN_EPI = false, bool SP2 = false>
; __device__ __forceinline__ void gemm_phase(PG8_LAS unsigned char* lds, const Gemm g, const Sched& S, const Epi& E, const int tid) {
;     ...
;             PG8_WAIT_V(8); PG8_WAIT_L(0); PG8_BAR; PG8_MMA(1, 0, At, B0); PG8_MMA(1, 1, At, B1); PG8_BAR; PG8_SCHED;
;             PG8_LDB(B0, 1, 0); PG8_LDB(B1, 1, 1); PG8_SCHED; PG8_LDA(At, 1, 0); PG8_STAGE(PG8_SA(0, 1), a2 + hstep, voffA);
;             PG8_WAIT_V(8); PG8_WAIT_L(0); PG8_BAR; PG8_MMA(0, 0, At, B0); PG8_MMA(0, 1, At, B1); PG8_BAR; PG8_SCHED;
;             PG8_LDA(At, 1, 1); PG8_STAGE(PG8_SB(1, 0), b3, voffB); PG8_STAGE(PG8_SB(1, 1), b3 + hstep, voffB); PG8_STAGE(PG8_SA(1, 0), a3, voffA);
	s_setprio 1
	s_waitcnt lgkmcnt(0)
	v_mfma_f32_16x16x32_bf16 v[62:65], v[132:135], v[188:191], v[62:65]
	v_mfma_f32_16x16x32_bf16 v[58:61], v[140:143], v[188:191], v[58:61]
	v_mfma_f32_16x16x32_bf16 v[50:53], v[132:135], v[198:201], v[50:53]
	v_mfma_f32_16x16x32_bf16 v[42:45], v[140:143], v[198:201], v[42:45]
	v_mfma_f32_16x16x32_bf16 v[34:37], v[132:135], v[206:209], v[34:37]
	v_mfma_f32_16x16x32_bf16 v[26:29], v[140:143], v[206:209], v[26:29]
	v_mfma_f32_16x16x32_bf16 v[18:21], v[132:135], v[214:217], v[18:21]
	v_mfma_f32_16x16x32_bf16 v[10:13], v[140:143], v[214:217], v[10:13]
	v_mfma_f32_16x16x32_bf16 v[62:65], v[136:139], v[192:195], v[62:65]
	v_mfma_f32_16x16x32_bf16 v[58:61], v[144:147], v[192:195], v[58:61]
	v_mfma_f32_16x16x32_bf16 v[50:53], v[136:139], v[202:205], v[50:53]
	v_mfma_f32_16x16x32_bf16 v[42:45], v[144:147], v[202:205], v[42:45]
	v_mfma_f32_16x16x32_bf16 v[34:37], v[136:139], v[210:213], v[34:37]
	v_mfma_f32_16x16x32_bf16 v[26:29], v[144:147], v[210:213], v[26:29]
	v_mfma_f32_16x16x32_bf16 v[18:21], v[136:139], v[218:221], v[18:21]
	v_mfma_f32_16x16x32_bf16 v[10:13], v[144:147], v[218:221], v[10:13]
	v_mfma_f32_16x16x32_bf16 v[54:57], v[172:175], v[188:191], v[54:57]
	v_mfma_f32_16x16x32_bf16 v[46:49], v[180:183], v[188:191], v[46:49]
	v_mfma_f32_16x16x32_bf16 v[38:41], v[172:175], v[198:201], v[38:41]
	v_mfma_f32_16x16x32_bf16 v[30:33], v[180:183], v[198:201], v[30:33]
	v_mfma_f32_16x16x32_bf16 v[22:25], v[172:175], v[206:209], v[22:25]
	v_mfma_f32_16x16x32_bf16 v[14:17], v[180:183], v[206:209], v[14:17]
	v_mfma_f32_16x16x32_bf16 v[6:9], v[172:175], v[214:217], v[6:9]
	v_mfma_f32_16x16x32_bf16 v[2:5], v[180:183], v[214:217], v[2:5]
	v_mfma_f32_16x16x32_bf16 v[54:57], v[176:179], v[192:195], v[54:57]
	v_mfma_f32_16x16x32_bf16 v[46:49], v[184:187], v[192:195], v[46:49]
	v_mfma_f32_16x16x32_bf16 v[38:41], v[176:179], v[202:205], v[38:41]
	v_mfma_f32_16x16x32_bf16 v[30:33], v[184:187], v[202:205], v[30:33]
	v_mfma_f32_16x16x32_bf16 v[22:25], v[176:179], v[210:213], v[22:25]
	v_mfma_f32_16x16x32_bf16 v[14:17], v[184:187], v[210:213], v[14:17]
	v_mfma_f32_16x16x32_bf16 v[6:9], v[176:179], v[218:221], v[6:9]
	v_mfma_f32_16x16x32_bf16 v[2:5], v[184:187], v[218:221], v[2:5]
	s_setprio 0
	s_barrier
	s_add_i32 s18, 0, 0x18000
	s_add_i32 s26, 0, 0x1c000
	v_add_u32_e32 v144, s18, v162
	v_add_u32_e32 v184, s26, v162
	ds_read_b128 v[132:135], v144
	ds_read_b128 v[136:139], v144 offset:1024
	ds_read_b128 v[140:143], v144 offset:2048
	ds_read_b128 v[144:147], v144 offset:3072
	ds_read_b128 v[172:175], v184
	ds_read_b128 v[176:179], v184 offset:1024
	ds_read_b128 v[180:183], v184 offset:2048
	ds_read_b128 v[184:187], v184 offset:3072
	s_add_u32 s22, s30, 0x160000
	s_addc_u32 s23, s31, 0
	s_mov_b32 m0, s46
	v_lshl_add_u64 v[228:229], s[22:23], 0, v[148:149]
	ds_read_b128 v[188:191], v171 offset:32768
	ds_read_b128 v[192:195], v171 offset:33792
	ds_read_b128 v[198:201], v171 offset:34816
	ds_read_b128 v[202:205], v171 offset:35840
	ds_read_b128 v[206:209], v171 offset:36864
	ds_read_b128 v[210:213], v171 offset:37888
	ds_read_b128 v[214:217], v171 offset:38912
	ds_read_b128 v[218:221], v171 offset:39936
	global_load_lds_dwordx4 v[228:229], off
	v_lshl_add_u64 v[228:229], s[22:23], 0, v[152:153]
	s_mov_b32 m0, s47
	s_nop 0
	global_load_lds_dwordx4 v[228:229], off
	s_waitcnt vmcnt(8)
	s_waitcnt lgkmcnt(0)
	s_barrier
	s_setprio 1
	s_waitcnt lgkmcnt(0)
	v_mfma_f32_16x16x32_bf16 v[126:129], v[132:135], v[188:191], v[126:129]
	v_mfma_f32_16x16x32_bf16 v[122:125], v[140:143], v[188:191], v[122:125]
	v_mfma_f32_16x16x32_bf16 v[114:117], v[132:135], v[198:201], v[114:117]
	v_mfma_f32_16x16x32_bf16 v[106:109], v[140:143], v[198:201], v[106:109]
	v_mfma_f32_16x16x32_bf16 v[98:101], v[132:135], v[206:209], v[98:101]
	v_mfma_f32_16x16x32_bf16 v[90:93], v[140:143], v[206:209], v[90:93]
	v_mfma_f32_16x16x32_bf16 v[82:85], v[132:135], v[214:217], v[82:85]
	v_mfma_f32_16x16x32_bf16 v[74:77], v[140:143], v[214:217], v[74:77]
	v_mfma_f32_16x16x32_bf16 v[126:129], v[136:139], v[192:195], v[126:129]
	v_mfma_f32_16x16x32_bf16 v[122:125], v[144:147], v[192:195], v[122:125]
	v_mfma_f32_16x16x32_bf16 v[114:117], v[136:139], v[202:205], v[114:117]
	v_mfma_f32_16x16x32_bf16 v[106:109], v[144:147], v[202:205], v[106:109]
	v_mfma_f32_16x16x32_bf16 v[98:101], v[136:139], v[210:213], v[98:101]
	v_mfma_f32_16x16x32_bf16 v[90:93], v[144:147], v[210:213], v[90:93]
	v_mfma_f32_16x16x32_bf16 v[82:85], v[136:139], v[218:221], v[82:85]
	v_mfma_f32_16x16x32_bf16 v[74:77], v[144:147], v[218:221], v[74:77]
	v_mfma_f32_16x16x32_bf16 v[118:121], v[172:175], v[188:191], v[118:121]
	v_mfma_f32_16x16x32_bf16 v[110:113], v[180:183], v[188:191], v[110:113]
	v_mfma_f32_16x16x32_bf16 v[102:105], v[172:175], v[198:201], v[102:105]
	v_mfma_f32_16x16x32_bf16 v[94:97], v[180:183], v[198:201], v[94:97]
	v_mfma_f32_16x16x32_bf16 v[86:89], v[172:175], v[206:209], v[86:89]
	v_mfma_f32_16x16x32_bf16 v[78:81], v[180:183], v[206:209], v[78:81]
	v_mfma_f32_16x16x32_bf16 v[70:73], v[172:175], v[214:217], v[70:73]
	v_mfma_f32_16x16x32_bf16 v[66:69], v[180:183], v[214:217], v[66:69]
	v_mfma_f32_16x16x32_bf16 v[118:121], v[176:179], v[192:195], v[118:121]
	v_mfma_f32_16x16x32_bf16 v[110:113], v[184:187], v[192:195], v[110:113]
	v_mfma_f32_16x16x32_bf16 v[102:105], v[176:179], v[202:205], v[102:105]
	v_mfma_f32_16x16x32_bf16 v[94:97], v[184:187], v[202:205], v[94:97]
	v_mfma_f32_16x16x32_bf16 v[86:89], v[176:179], v[210:213], v[86:89]
	v_mfma_f32_16x16x32_bf16 v[78:81], v[184:187], v[210:213], v[78:81]
	v_mfma_f32_16x16x32_bf16 v[70:73], v[176:179], v[218:221], v[70:73]
	v_mfma_f32_16x16x32_bf16 v[66:69], v[184:187], v[218:221], v[66:69]
	s_setprio 0
	s_barrier
; #define PG8_STAGE(bufoff, gbase, voff) do { _Pragma("unroll") for (int _i = 0; _i < 2; ++_i) \
;         __builtin_amdgcn_global_load_lds((const unsigned*)((const char*)(gbase) + (voff)[_i]), (PG8_LAS unsigned*)(lds + (bufoff) + ldsw + _i * 8192), 16, 0, 0); } while (0)
; #define PG8_LDA(dst, b, h) do { _Pragma("unroll") for (int m = 0; m < 4; ++m) _Pragma("unroll") for (int k = 0; k < 2; ++k) dst[m][k] = *(const PG8_LAS bf16x8*)(lds + PG8_SA(b, h) + aoff + m * 2048 + k * 1024); } while (0)
; #define PG8_MMA(ai, bj, At, Bt) do { __builtin_amdgcn_s_setprio(1); _Pragma("unroll") for (int m = 0; m < 4; ++m) _Pragma("unroll") for (int n = 0; n < 2; ++n) _Pragma("unroll") for (int k = 0; k < 2; ++k) \
;         acc[ai][bj][m][n] = __builtin_amdgcn_mfma_f32_16x16x32_bf16(Bt[n][k], At[m][k], acc[ai][bj][m][n], 0, 0, 0); __builtin_amdgcn_s_setprio(0); } while (0)
; #define PG8_WAIT_V(n) asm volatile("s_waitcnt vmcnt(" #n ")" ::: "memory")
; #define PG8_WAIT_L(n) asm volatile("s_waitcnt lgkmcnt(" #n ")" ::: "memory")
; #define PG8_BAR __builtin_amdgcn_s_barrier()
; #define PG8_SCHED __builtin_amdgcn_sched_barrier(0)
; #define PG8_STAGE(bufoff, gbase, voff) do { _Pragma("unroll") for (int _i = 0; _i < 2; ++_i) \
;         __builtin_amdgcn_global_load_lds((const unsigned*)((const char*)(gbase) + (voff)[_i]), (PG8_LAS unsigned*)(lds + (bufoff) + ldsw + _i * 8192), 16, 0, 0); } while (0)
; #define PG8_LDA(dst, b, h) do { _Pragma("unroll") for (int mb = 0; mb < 2; ++mb) _Pragma("unroll") for (int s = 0; s < 2; ++s) \
;         dst[mb][s] = cat8(*(const PG8_LAS bf16x8*)(lds + PG8_SA(b, h) + aoffk[s][0] + mb * 4096), *(const PG8_LAS bf16x8*)(lds + PG8_SA(b, h) + aoffk[s][1] + mb * 4096)); } while (0)
; template <class Epi, class Sched, bool ALIGN_EPI = false, bool SP2 = false>
; __device__ __forceinline__ void gemm_phase(PG8_LAS unsigned char* lds, const Gemm g, const Sched& S, const Epi& E, const int tid) {
;     ...
;         for (int t = 0; t < nt; t += 2) {
;     ...
;             PG8_WAIT_V(8); PG8_WAIT_L(0); PG8_BAR; PG8_MMA(0, 0, At, B0); PG8_MMA(0, 1, At, B1); PG8_BAR; PG8_SCHED;
;             PG8_LDA(At, 1, 1); PG8_STAGE(PG8_SB(1, 0), b3, voffB); PG8_STAGE(PG8_SB(1, 1), b3 + hstep, voffB); PG8_STAGE(PG8_SA(1, 0), a3, voffA);
;             PG8_WAIT_V(8); PG8_WAIT_L(0); PG8_BAR; PG8_MMA(1, 0, At, B0); PG8_MMA(1, 1, At, B1); PG8_BAR; PG8_SCHED;
	s_add_i32 s18, s18, s43
	v_lshl_add_u64 v[160:161], v[160:161], 0, s[34:35]
	s_mov_b32 m0, s18
	ds_read_b128 v[188:191], v171 offset:49152
	ds_read_b128 v[192:195], v171 offset:50176
	ds_read_b128 v[198:201], v171 offset:51200
	ds_read_b128 v[202:205], v171 offset:52224
	ds_read_b128 v[206:209], v171 offset:53248
	ds_read_b128 v[210:213], v171 offset:54272
	ds_read_b128 v[214:217], v171 offset:55296
	ds_read_b128 v[218:221], v171 offset:56320
	global_load_lds_dwordx4 v[160:161], off
	s_add_i32 m0, s18, 0x2000
	s_add_u32 s22, s28, 0x160080
	v_lshl_add_u64 v[160:161], v[222:223], 0, s[34:35]
	s_addc_u32 s23, s29, 0
	s_add_i32 s18, s26, s43
	global_load_lds_dwordx4 v[160:161], off
	v_lshl_add_u64 v[160:161], s[22:23], 0, v[150:151]
	s_mov_b32 m0, s18
	s_nop 0
	global_load_lds_dwordx4 v[160:161], off
	v_lshl_add_u64 v[160:161], s[22:23], 0, v[154:155]
	s_add_i32 m0, s18, 0x2000
	s_nop 0
	global_load_lds_dwordx4 v[160:161], off
	v_lshl_add_u64 v[160:161], v[224:225], 0, s[34:35]
	s_mov_b32 m0, s48
	s_nop 0
	global_load_lds_dwordx4 v[160:161], off
	v_lshl_add_u64 v[160:161], v[226:227], 0, s[34:35]
	s_mov_b32 m0, s49
	s_nop 0
	global_load_lds_dwordx4 v[160:161], off
	s_waitcnt vmcnt(8)
	s_waitcnt lgkmcnt(0)
	s_barrier
	s_setprio 1
	s_waitcnt lgkmcnt(0)
	v_mfma_f32_16x16x32_bf16 v[62:65], v[132:135], v[188:191], v[62:65]
	v_mfma_f32_16x16x32_bf16 v[58:61], v[140:143], v[188:191], v[58:61]
	v_mfma_f32_16x16x32_bf16 v[50:53], v[132:135], v[198:201], v[50:53]
	v_mfma_f32_16x16x32_bf16 v[42:45], v[140:143], v[198:201], v[42:45]
	v_mfma_f32_16x16x32_bf16 v[34:37], v[132:135], v[206:209], v[34:37]
	v_mfma_f32_16x16x32_bf16 v[26:29], v[140:143], v[206:209], v[26:29]
	v_mfma_f32_16x16x32_bf16 v[18:21], v[132:135], v[214:217], v[18:21]
	v_mfma_f32_16x16x32_bf16 v[10:13], v[140:143], v[214:217], v[10:13]
	v_mfma_f32_16x16x32_bf16 v[62:65], v[136:139], v[192:195], v[62:65]
	v_mfma_f32_16x16x32_bf16 v[58:61], v[144:147], v[192:195], v[58:61]
	v_mfma_f32_16x16x32_bf16 v[50:53], v[136:139], v[202:205], v[50:53]
	v_mfma_f32_16x16x32_bf16 v[42:45], v[144:147], v[202:205], v[42:45]
	v_mfma_f32_16x16x32_bf16 v[34:37], v[136:139], v[210:213], v[34:37]
	v_mfma_f32_16x16x32_bf16 v[26:29], v[144:147], v[210:213], v[26:29]
	v_mfma_f32_16x16x32_bf16 v[18:21], v[136:139], v[218:221], v[18:21]
	v_mfma_f32_16x16x32_bf16 v[10:13], v[144:147], v[218:221], v[10:13]
	v_mfma_f32_16x16x32_bf16 v[54:57], v[172:175], v[188:191], v[54:57]
	v_mfma_f32_16x16x32_bf16 v[46:49], v[180:183], v[188:191], v[46:49]
	v_mfma_f32_16x16x32_bf16 v[38:41], v[172:175], v[198:201], v[38:41]
	v_mfma_f32_16x16x32_bf16 v[30:33], v[180:183], v[198:201], v[30:33]
	v_mfma_f32_16x16x32_bf16 v[22:25], v[172:175], v[206:209], v[22:25]
	v_mfma_f32_16x16x32_bf16 v[14:17], v[180:183], v[206:209], v[14:17]
	v_mfma_f32_16x16x32_bf16 v[6:9], v[172:175], v[214:217], v[6:9]
	v_mfma_f32_16x16x32_bf16 v[2:5], v[180:183], v[214:217], v[2:5]
	v_mfma_f32_16x16x32_bf16 v[54:57], v[176:179], v[192:195], v[54:57]
	v_mfma_f32_16x16x32_bf16 v[46:49], v[184:187], v[192:195], v[46:49]
	v_mfma_f32_16x16x32_bf16 v[38:41], v[176:179], v[202:205], v[38:41]
	v_mfma_f32_16x16x32_bf16 v[30:33], v[184:187], v[202:205], v[30:33]
	v_mfma_f32_16x16x32_bf16 v[22:25], v[176:179], v[210:213], v[22:25]
	v_mfma_f32_16x16x32_bf16 v[14:17], v[184:187], v[210:213], v[14:17]
	v_mfma_f32_16x16x32_bf16 v[6:9], v[176:179], v[218:221], v[6:9]
	v_mfma_f32_16x16x32_bf16 v[2:5], v[184:187], v[218:221], v[2:5]
	s_setprio 0
	s_barrier
	s_add_u32 s13, s13, 0x100
	s_addc_u32 s15, s15, 0
	s_cmp_ge_i32 s19, s2
	s_mov_b64 s[22:23], s[6:7]
	s_mov_b32 s18, s19
	s_cbranch_scc0 .LBB0_2525
	s_and_b64 vcc, exec, s[10:11]
	s_cbranch_vccz .LBB0_2528
	s_barrier
